# speedup vs baseline: 1.0506x; 1.0052x over previous
.LBB1_25:
	s_or_b64 exec, exec, s[10:11]
	s_load_dwordx2 s[0:1], s[0:1], 0x18
	v_lshl_or_b32 v2, s2, 14, v0
	s_mov_b32 s3, 0x155cc0
	v_cmp_gt_i32_e32 vcc, s3, v2
	v_mov_b32_e32 v1, -1
	s_waitcnt lgkmcnt(0)
	s_barrier
	s_mov_b32 s10, 0x61a80
	s_mov_b32 s11, 0xf4240
	s_mov_b32 s12, 0x155cc0
	v_mov_b32_e32 v21, s4
	v_mov_b32_e32 v22, s5
	v_mov_b32_e32 v23, s6
	v_mov_b32_e32 v24, s7
	v_mov_b32_e32 v25, s8
	v_mov_b32_e32 v26, s9
	v_mov_b32_e32 v29, 0
	v_mov_b32_e32 v33, 0
	v_mov_b32_e32 v35, 0x30d40
	v_mov_b32_e32 v36, 0xfff6d840
	v_mov_b32_e32 v34, 0x61a80
	v_mov_b32_e32 v37, 0x61a80
	v_mov_b32_e32 v38, 0xf4240
	v_mov_b32_e32 v39, 0x30d40
	v_mov_b32_e32 v40, 0x61a80
	v_cmp_gt_u32_e64 s[14:15], s10, v2
	v_cmp_gt_u32_e64 s[16:17], s11, v2
	v_cmp_gt_u32_e64 s[18:19], s12, v2
	s_nop 0
	v_cndmask_b32_e64 v30, v25, v23, s[16:17]
	v_cndmask_b32_e64 v30, v30, v21, s[14:15]
	v_cndmask_b32_e64 v31, v26, v24, s[16:17]
	v_cndmask_b32_e64 v31, v31, v22, s[14:15]
	v_cndmask_b32_e64 v28, v36, v35, s[16:17]
	v_cndmask_b32_e64 v28, v28, v34, s[14:15]
	v_add_u32_e32 v28, v28, v2
	v_cndmask_b32_e64 v28, 0, v28, s[18:19]
	v_lshl_add_u64 v[32:33], v[28:29], 2, v[30:31]
	global_load_dword v1, v[32:33], off
	v_add_u32_e32 v27, 0x400, v2
	v_cmp_gt_u32_e64 s[14:15], s10, v27
	v_cmp_gt_u32_e64 s[16:17], s11, v27
	v_cmp_gt_u32_e64 s[18:19], s12, v27
	s_nop 0
	v_cndmask_b32_e64 v30, v25, v23, s[16:17]
	v_cndmask_b32_e64 v30, v30, v21, s[14:15]
	v_cndmask_b32_e64 v31, v26, v24, s[16:17]
	v_cndmask_b32_e64 v31, v31, v22, s[14:15]
	v_cndmask_b32_e64 v28, v36, v35, s[16:17]
	v_cndmask_b32_e64 v28, v28, v34, s[14:15]
	v_add_u32_e32 v28, v28, v27
	v_cndmask_b32_e64 v28, 0, v28, s[18:19]
	v_lshl_add_u64 v[32:33], v[28:29], 2, v[30:31]
	global_load_dword v7, v[32:33], off
	v_add_u32_e32 v27, 0x800, v2
	v_cmp_gt_u32_e64 s[14:15], s10, v27
	v_cmp_gt_u32_e64 s[16:17], s11, v27
	v_cmp_gt_u32_e64 s[18:19], s12, v27
	s_nop 0
	v_cndmask_b32_e64 v30, v25, v23, s[16:17]
	v_cndmask_b32_e64 v30, v30, v21, s[14:15]
	v_cndmask_b32_e64 v31, v26, v24, s[16:17]
	v_cndmask_b32_e64 v31, v31, v22, s[14:15]
	v_cndmask_b32_e64 v28, v36, v35, s[16:17]
	v_cndmask_b32_e64 v28, v28, v34, s[14:15]
	v_add_u32_e32 v28, v28, v27
	v_cndmask_b32_e64 v28, 0, v28, s[18:19]
	v_lshl_add_u64 v[32:33], v[28:29], 2, v[30:31]
	global_load_dword v8, v[32:33], off
	v_add_u32_e32 v27, 0xc00, v2
	v_cmp_gt_u32_e64 s[14:15], s10, v27
	v_cmp_gt_u32_e64 s[16:17], s11, v27
	v_cmp_gt_u32_e64 s[18:19], s12, v27
	s_nop 0
	v_cndmask_b32_e64 v30, v25, v23, s[16:17]
	v_cndmask_b32_e64 v30, v30, v21, s[14:15]
	v_cndmask_b32_e64 v31, v26, v24, s[16:17]
	v_cndmask_b32_e64 v31, v31, v22, s[14:15]
	v_cndmask_b32_e64 v28, v36, v35, s[16:17]
	v_cndmask_b32_e64 v28, v28, v34, s[14:15]
	v_add_u32_e32 v28, v28, v27
	v_cndmask_b32_e64 v28, 0, v28, s[18:19]
	v_lshl_add_u64 v[32:33], v[28:29], 2, v[30:31]
	global_load_dword v9, v[32:33], off
	v_add_u32_e32 v27, 0x1000, v2
	v_cmp_gt_u32_e64 s[14:15], s10, v27
	v_cmp_gt_u32_e64 s[16:17], s11, v27
	v_cmp_gt_u32_e64 s[18:19], s12, v27
	s_nop 0
	v_cndmask_b32_e64 v30, v25, v23, s[16:17]
	v_cndmask_b32_e64 v30, v30, v21, s[14:15]
	v_cndmask_b32_e64 v31, v26, v24, s[16:17]
	v_cndmask_b32_e64 v31, v31, v22, s[14:15]
	v_cndmask_b32_e64 v28, v36, v35, s[16:17]
	v_cndmask_b32_e64 v28, v28, v34, s[14:15]
	v_add_u32_e32 v28, v28, v27
	v_cndmask_b32_e64 v28, 0, v28, s[18:19]
	v_lshl_add_u64 v[32:33], v[28:29], 2, v[30:31]
	global_load_dword v10, v[32:33], off
	v_add_u32_e32 v27, 0x1400, v2
	v_cmp_gt_u32_e64 s[14:15], s10, v27
	v_cmp_gt_u32_e64 s[16:17], s11, v27
	v_cmp_gt_u32_e64 s[18:19], s12, v27
	s_nop 0
	v_cndmask_b32_e64 v30, v25, v23, s[16:17]
	v_cndmask_b32_e64 v30, v30, v21, s[14:15]
	v_cndmask_b32_e64 v31, v26, v24, s[16:17]
	v_cndmask_b32_e64 v31, v31, v22, s[14:15]
	v_cndmask_b32_e64 v28, v36, v35, s[16:17]
	v_cndmask_b32_e64 v28, v28, v34, s[14:15]
	v_add_u32_e32 v28, v28, v27
	v_cndmask_b32_e64 v28, 0, v28, s[18:19]
	v_lshl_add_u64 v[32:33], v[28:29], 2, v[30:31]
	global_load_dword v11, v[32:33], off
	v_add_u32_e32 v27, 0x1800, v2
	v_cmp_gt_u32_e64 s[14:15], s10, v27
	v_cmp_gt_u32_e64 s[16:17], s11, v27
	v_cmp_gt_u32_e64 s[18:19], s12, v27
	s_nop 0
	v_cndmask_b32_e64 v30, v25, v23, s[16:17]
	v_cndmask_b32_e64 v30, v30, v21, s[14:15]
	v_cndmask_b32_e64 v31, v26, v24, s[16:17]
	v_cndmask_b32_e64 v31, v31, v22, s[14:15]
	v_cndmask_b32_e64 v28, v36, v35, s[16:17]
	v_cndmask_b32_e64 v28, v28, v34, s[14:15]
	v_add_u32_e32 v28, v28, v27
	v_cndmask_b32_e64 v28, 0, v28, s[18:19]
	v_lshl_add_u64 v[32:33], v[28:29], 2, v[30:31]
	global_load_dword v12, v[32:33], off
	v_add_u32_e32 v27, 0x1c00, v2
	v_cmp_gt_u32_e64 s[14:15], s10, v27
	v_cmp_gt_u32_e64 s[16:17], s11, v27
	v_cmp_gt_u32_e64 s[18:19], s12, v27
	s_nop 0
	v_cndmask_b32_e64 v30, v25, v23, s[16:17]
	v_cndmask_b32_e64 v30, v30, v21, s[14:15]
	v_cndmask_b32_e64 v31, v26, v24, s[16:17]
	v_cndmask_b32_e64 v31, v31, v22, s[14:15]
	v_cndmask_b32_e64 v28, v36, v35, s[16:17]
	v_cndmask_b32_e64 v28, v28, v34, s[14:15]
	v_add_u32_e32 v28, v28, v27
	v_cndmask_b32_e64 v28, 0, v28, s[18:19]
	v_lshl_add_u64 v[32:33], v[28:29], 2, v[30:31]
	global_load_dword v13, v[32:33], off
	v_add_u32_e32 v27, 0x2000, v2
	v_cmp_gt_u32_e64 s[14:15], s10, v27
	v_cmp_gt_u32_e64 s[16:17], s11, v27
	v_cmp_gt_u32_e64 s[18:19], s12, v27
	s_nop 0
	v_cndmask_b32_e64 v30, v25, v23, s[16:17]
	v_cndmask_b32_e64 v30, v30, v21, s[14:15]
	v_cndmask_b32_e64 v31, v26, v24, s[16:17]
	v_cndmask_b32_e64 v31, v31, v22, s[14:15]
	v_cndmask_b32_e64 v28, v36, v35, s[16:17]
	v_cndmask_b32_e64 v28, v28, v34, s[14:15]
	v_add_u32_e32 v28, v28, v27
	v_cndmask_b32_e64 v28, 0, v28, s[18:19]
	v_lshl_add_u64 v[32:33], v[28:29], 2, v[30:31]
	global_load_dword v14, v[32:33], off
	v_add_u32_e32 v27, 0x2400, v2
	v_cmp_gt_u32_e64 s[14:15], s10, v27
	v_cmp_gt_u32_e64 s[16:17], s11, v27
	v_cmp_gt_u32_e64 s[18:19], s12, v27
	s_nop 0
	v_cndmask_b32_e64 v30, v25, v23, s[16:17]
	v_cndmask_b32_e64 v30, v30, v21, s[14:15]
	v_cndmask_b32_e64 v31, v26, v24, s[16:17]
	v_cndmask_b32_e64 v31, v31, v22, s[14:15]
	v_cndmask_b32_e64 v28, v36, v35, s[16:17]
	v_cndmask_b32_e64 v28, v28, v34, s[14:15]
	v_add_u32_e32 v28, v28, v27
	v_cndmask_b32_e64 v28, 0, v28, s[18:19]
	v_lshl_add_u64 v[32:33], v[28:29], 2, v[30:31]
	global_load_dword v15, v[32:33], off
	v_add_u32_e32 v27, 0x2800, v2
	v_cmp_gt_u32_e64 s[14:15], s10, v27
	v_cmp_gt_u32_e64 s[16:17], s11, v27
	v_cmp_gt_u32_e64 s[18:19], s12, v27
	s_nop 0
	v_cndmask_b32_e64 v30, v25, v23, s[16:17]
	v_cndmask_b32_e64 v30, v30, v21, s[14:15]
	v_cndmask_b32_e64 v31, v26, v24, s[16:17]
	v_cndmask_b32_e64 v31, v31, v22, s[14:15]
	v_cndmask_b32_e64 v28, v36, v35, s[16:17]
	v_cndmask_b32_e64 v28, v28, v34, s[14:15]
	v_add_u32_e32 v28, v28, v27
	v_cndmask_b32_e64 v28, 0, v28, s[18:19]
	v_lshl_add_u64 v[32:33], v[28:29], 2, v[30:31]
	global_load_dword v16, v[32:33], off
	v_add_u32_e32 v27, 0x2c00, v2
	v_cmp_gt_u32_e64 s[14:15], s10, v27
	v_cmp_gt_u32_e64 s[16:17], s11, v27
	v_cmp_gt_u32_e64 s[18:19], s12, v27
	s_nop 0
	v_cndmask_b32_e64 v30, v25, v23, s[16:17]
	v_cndmask_b32_e64 v30, v30, v21, s[14:15]
	v_cndmask_b32_e64 v31, v26, v24, s[16:17]
	v_cndmask_b32_e64 v31, v31, v22, s[14:15]
	v_cndmask_b32_e64 v28, v36, v35, s[16:17]
	v_cndmask_b32_e64 v28, v28, v34, s[14:15]
	v_add_u32_e32 v28, v28, v27
	v_cndmask_b32_e64 v28, 0, v28, s[18:19]
	v_lshl_add_u64 v[32:33], v[28:29], 2, v[30:31]
	global_load_dword v17, v[32:33], off
	v_add_u32_e32 v27, 0x3000, v2
	v_cmp_gt_u32_e64 s[14:15], s10, v27
	v_cmp_gt_u32_e64 s[16:17], s11, v27
	v_cmp_gt_u32_e64 s[18:19], s12, v27
	s_nop 0
	v_cndmask_b32_e64 v30, v25, v23, s[16:17]
	v_cndmask_b32_e64 v30, v30, v21, s[14:15]
	v_cndmask_b32_e64 v31, v26, v24, s[16:17]
	v_cndmask_b32_e64 v31, v31, v22, s[14:15]
	v_cndmask_b32_e64 v28, v36, v35, s[16:17]
	v_cndmask_b32_e64 v28, v28, v34, s[14:15]
	v_add_u32_e32 v28, v28, v27
	v_cndmask_b32_e64 v28, 0, v28, s[18:19]
	v_lshl_add_u64 v[32:33], v[28:29], 2, v[30:31]
	global_load_dword v18, v[32:33], off
	v_add_u32_e32 v27, 0x3400, v2
	v_cmp_gt_u32_e64 s[14:15], s10, v27
	v_cmp_gt_u32_e64 s[16:17], s11, v27
	v_cmp_gt_u32_e64 s[18:19], s12, v27
	s_nop 0
	v_cndmask_b32_e64 v30, v25, v23, s[16:17]
	v_cndmask_b32_e64 v30, v30, v21, s[14:15]
	v_cndmask_b32_e64 v31, v26, v24, s[16:17]
	v_cndmask_b32_e64 v31, v31, v22, s[14:15]
	v_cndmask_b32_e64 v28, v36, v35, s[16:17]
	v_cndmask_b32_e64 v28, v28, v34, s[14:15]
	v_add_u32_e32 v28, v28, v27
	v_cndmask_b32_e64 v28, 0, v28, s[18:19]
	v_lshl_add_u64 v[32:33], v[28:29], 2, v[30:31]
	global_load_dword v19, v[32:33], off
	v_add_u32_e32 v27, 0x3800, v2
	v_cmp_gt_u32_e64 s[14:15], s10, v27
	v_cmp_gt_u32_e64 s[16:17], s11, v27
	v_cmp_gt_u32_e64 s[18:19], s12, v27
	s_nop 0
	v_cndmask_b32_e64 v30, v25, v23, s[16:17]
	v_cndmask_b32_e64 v30, v30, v21, s[14:15]
	v_cndmask_b32_e64 v31, v26, v24, s[16:17]
	v_cndmask_b32_e64 v31, v31, v22, s[14:15]
	v_cndmask_b32_e64 v28, v36, v35, s[16:17]
	v_cndmask_b32_e64 v28, v28, v34, s[14:15]
	v_add_u32_e32 v28, v28, v27
	v_cndmask_b32_e64 v28, 0, v28, s[18:19]
	v_lshl_add_u64 v[32:33], v[28:29], 2, v[30:31]
	global_load_dword v20, v[32:33], off
	v_add_u32_e32 v27, 0x3c00, v2
	v_cmp_gt_u32_e64 s[14:15], s10, v27
	v_cmp_gt_u32_e64 s[16:17], s11, v27
	v_cmp_gt_u32_e64 s[18:19], s12, v27
	s_nop 0
	v_cndmask_b32_e64 v30, v25, v23, s[16:17]
	v_cndmask_b32_e64 v30, v30, v21, s[14:15]
	v_cndmask_b32_e64 v31, v26, v24, s[16:17]
	v_cndmask_b32_e64 v31, v31, v22, s[14:15]
	v_cndmask_b32_e64 v28, v36, v35, s[16:17]
	v_cndmask_b32_e64 v28, v28, v34, s[14:15]
	v_add_u32_e32 v28, v28, v27
	v_cndmask_b32_e64 v28, 0, v28, s[18:19]
	v_lshl_add_u64 v[32:33], v[28:29], 2, v[30:31]
	global_load_dword v4, v[32:33], off
	s_waitcnt vmcnt(0)
	v_mov_b32_e32 v30, -1
	v_cmp_gt_u32_e64 s[14:15], s10, v2
	v_cmp_gt_u32_e64 s[16:17], s11, v2
	v_cmp_gt_u32_e64 s[18:19], s12, v2
	s_nop 0
	v_cndmask_b32_e64 v28, v40, v39, s[16:17]
	v_cndmask_b32_e64 v28, v28, 0, s[14:15]
	v_add_u32_e32 v1, v1, v28
	v_cndmask_b32_e64 v1, v30, v1, s[18:19]
	v_add_u32_e32 v27, 0x400, v2
	v_cmp_gt_u32_e64 s[14:15], s10, v27
	v_cmp_gt_u32_e64 s[16:17], s11, v27
	v_cmp_gt_u32_e64 s[18:19], s12, v27
	s_nop 0
	v_cndmask_b32_e64 v28, v40, v39, s[16:17]
	v_cndmask_b32_e64 v28, v28, 0, s[14:15]
	v_add_u32_e32 v7, v7, v28
	v_cndmask_b32_e64 v7, v30, v7, s[18:19]
	v_add_u32_e32 v27, 0x800, v2
	v_cmp_gt_u32_e64 s[14:15], s10, v27
	v_cmp_gt_u32_e64 s[16:17], s11, v27
	v_cmp_gt_u32_e64 s[18:19], s12, v27
	s_nop 0
	v_cndmask_b32_e64 v28, v40, v39, s[16:17]
	v_cndmask_b32_e64 v28, v28, 0, s[14:15]
	v_add_u32_e32 v8, v8, v28
	v_cndmask_b32_e64 v8, v30, v8, s[18:19]
	v_add_u32_e32 v27, 0xc00, v2
	v_cmp_gt_u32_e64 s[14:15], s10, v27
	v_cmp_gt_u32_e64 s[16:17], s11, v27
	v_cmp_gt_u32_e64 s[18:19], s12, v27
	s_nop 0
	v_cndmask_b32_e64 v28, v40, v39, s[16:17]
	v_cndmask_b32_e64 v28, v28, 0, s[14:15]
	v_add_u32_e32 v9, v9, v28
	v_cndmask_b32_e64 v9, v30, v9, s[18:19]
	v_add_u32_e32 v27, 0x1000, v2
	v_cmp_gt_u32_e64 s[14:15], s10, v27
	v_cmp_gt_u32_e64 s[16:17], s11, v27
	v_cmp_gt_u32_e64 s[18:19], s12, v27
	s_nop 0
	v_cndmask_b32_e64 v28, v40, v39, s[16:17]
	v_cndmask_b32_e64 v28, v28, 0, s[14:15]
	v_add_u32_e32 v10, v10, v28
	v_cndmask_b32_e64 v10, v30, v10, s[18:19]
	v_add_u32_e32 v27, 0x1400, v2
	v_cmp_gt_u32_e64 s[14:15], s10, v27
	v_cmp_gt_u32_e64 s[16:17], s11, v27
	v_cmp_gt_u32_e64 s[18:19], s12, v27
	s_nop 0
	v_cndmask_b32_e64 v28, v40, v39, s[16:17]
	v_cndmask_b32_e64 v28, v28, 0, s[14:15]
	v_add_u32_e32 v11, v11, v28
	v_cndmask_b32_e64 v11, v30, v11, s[18:19]
	v_add_u32_e32 v27, 0x1800, v2
	v_cmp_gt_u32_e64 s[14:15], s10, v27
	v_cmp_gt_u32_e64 s[16:17], s11, v27
	v_cmp_gt_u32_e64 s[18:19], s12, v27
	s_nop 0
	v_cndmask_b32_e64 v28, v40, v39, s[16:17]
	v_cndmask_b32_e64 v28, v28, 0, s[14:15]
	v_add_u32_e32 v12, v12, v28
	v_cndmask_b32_e64 v12, v30, v12, s[18:19]
	v_add_u32_e32 v27, 0x1c00, v2
	v_cmp_gt_u32_e64 s[14:15], s10, v27
	v_cmp_gt_u32_e64 s[16:17], s11, v27
	v_cmp_gt_u32_e64 s[18:19], s12, v27
	s_nop 0
	v_cndmask_b32_e64 v28, v40, v39, s[16:17]
	v_cndmask_b32_e64 v28, v28, 0, s[14:15]
	v_add_u32_e32 v13, v13, v28
	v_cndmask_b32_e64 v13, v30, v13, s[18:19]
	v_add_u32_e32 v27, 0x2000, v2
	v_cmp_gt_u32_e64 s[14:15], s10, v27
	v_cmp_gt_u32_e64 s[16:17], s11, v27
	v_cmp_gt_u32_e64 s[18:19], s12, v27
	s_nop 0
	v_cndmask_b32_e64 v28, v40, v39, s[16:17]
	v_cndmask_b32_e64 v28, v28, 0, s[14:15]
	v_add_u32_e32 v14, v14, v28
	v_cndmask_b32_e64 v14, v30, v14, s[18:19]
	v_add_u32_e32 v27, 0x2400, v2
	v_cmp_gt_u32_e64 s[14:15], s10, v27
	v_cmp_gt_u32_e64 s[16:17], s11, v27
	v_cmp_gt_u32_e64 s[18:19], s12, v27
	s_nop 0
	v_cndmask_b32_e64 v28, v40, v39, s[16:17]
	v_cndmask_b32_e64 v28, v28, 0, s[14:15]
	v_add_u32_e32 v15, v15, v28
	v_cndmask_b32_e64 v15, v30, v15, s[18:19]
	v_add_u32_e32 v27, 0x2800, v2
	v_cmp_gt_u32_e64 s[14:15], s10, v27
	v_cmp_gt_u32_e64 s[16:17], s11, v27
	v_cmp_gt_u32_e64 s[18:19], s12, v27
	s_nop 0
	v_cndmask_b32_e64 v28, v40, v39, s[16:17]
	v_cndmask_b32_e64 v28, v28, 0, s[14:15]
	v_add_u32_e32 v16, v16, v28
	v_cndmask_b32_e64 v16, v30, v16, s[18:19]
	v_add_u32_e32 v27, 0x2c00, v2
	v_cmp_gt_u32_e64 s[14:15], s10, v27
	v_cmp_gt_u32_e64 s[16:17], s11, v27
	v_cmp_gt_u32_e64 s[18:19], s12, v27
	s_nop 0
	v_cndmask_b32_e64 v28, v40, v39, s[16:17]
	v_cndmask_b32_e64 v28, v28, 0, s[14:15]
	v_add_u32_e32 v17, v17, v28
	v_cndmask_b32_e64 v17, v30, v17, s[18:19]
	v_add_u32_e32 v27, 0x3000, v2
	v_cmp_gt_u32_e64 s[14:15], s10, v27
	v_cmp_gt_u32_e64 s[16:17], s11, v27
	v_cmp_gt_u32_e64 s[18:19], s12, v27
	s_nop 0
	v_cndmask_b32_e64 v28, v40, v39, s[16:17]
	v_cndmask_b32_e64 v28, v28, 0, s[14:15]
	v_add_u32_e32 v18, v18, v28
	v_cndmask_b32_e64 v18, v30, v18, s[18:19]
	v_add_u32_e32 v27, 0x3400, v2
	v_cmp_gt_u32_e64 s[14:15], s10, v27
	v_cmp_gt_u32_e64 s[16:17], s11, v27
	v_cmp_gt_u32_e64 s[18:19], s12, v27
	s_nop 0
	v_cndmask_b32_e64 v28, v40, v39, s[16:17]
	v_cndmask_b32_e64 v28, v28, 0, s[14:15]
	v_add_u32_e32 v19, v19, v28
	v_cndmask_b32_e64 v19, v30, v19, s[18:19]
	v_add_u32_e32 v27, 0x3800, v2
	v_cmp_gt_u32_e64 s[14:15], s10, v27
	v_cmp_gt_u32_e64 s[16:17], s11, v27
	v_cmp_gt_u32_e64 s[18:19], s12, v27
	s_nop 0
	v_cndmask_b32_e64 v28, v40, v39, s[16:17]
	v_cndmask_b32_e64 v28, v28, 0, s[14:15]
	v_add_u32_e32 v20, v20, v28
	v_cndmask_b32_e64 v20, v30, v20, s[18:19]
	v_add_u32_e32 v27, 0x3c00, v2
	v_cmp_gt_u32_e64 s[14:15], s10, v27
	v_cmp_gt_u32_e64 s[16:17], s11, v27
	v_cmp_gt_u32_e64 s[18:19], s12, v27
	s_nop 0
	v_cndmask_b32_e64 v28, v40, v39, s[16:17]
	v_cndmask_b32_e64 v28, v28, 0, s[14:15]
	v_add_u32_e32 v4, v4, v28
	v_cndmask_b32_e64 v4, v30, v4, s[18:19]
	s_waitcnt vmcnt(0)
	v_cmp_lt_i32_e32 vcc, -1, v1
	s_and_saveexec_b64 s[4:5], vcc
	s_cbranch_execnz .LBB1_205

	.amdhsa_kernel _Z8k_bcountPKiS0_S0_PiPjPKfS4_S0_S0_S0_S4_S4_S4_PDF16_S5_
		.amdhsa_group_segment_fixed_size 4384
		.amdhsa_private_segment_fixed_size 0
		.amdhsa_kernarg_size 120
		.amdhsa_user_sgpr_count 2
		.amdhsa_user_sgpr_dispatch_ptr 0
		.amdhsa_user_sgpr_queue_ptr 0
		.amdhsa_user_sgpr_kernarg_segment_ptr 1
		.amdhsa_user_sgpr_dispatch_id 0
		.amdhsa_user_sgpr_kernarg_preload_length 0
		.amdhsa_user_sgpr_kernarg_preload_offset 0
		.amdhsa_user_sgpr_private_segment_size 0
		.amdhsa_uses_dynamic_stack 0
		.amdhsa_enable_private_segment 0
		.amdhsa_system_sgpr_workgroup_id_x 1
		.amdhsa_system_sgpr_workgroup_id_y 0
		.amdhsa_system_sgpr_workgroup_id_z 0
		.amdhsa_system_sgpr_workgroup_info 0
		.amdhsa_system_vgpr_workitem_id 0
		.amdhsa_next_free_vgpr 41
		.amdhsa_next_free_sgpr 20
		.amdhsa_accum_offset 44
		.amdhsa_reserve_vcc 1
		.amdhsa_float_round_mode_32 0
		.amdhsa_float_round_mode_16_64 0
		.amdhsa_float_denorm_mode_32 3
		.amdhsa_float_denorm_mode_16_64 3
		.amdhsa_dx10_clamp 1
		.amdhsa_ieee_mode 1
		.amdhsa_fp16_overflow 0
		.amdhsa_tg_split 0
		.amdhsa_exception_fp_ieee_invalid_op 0
		.amdhsa_exception_fp_denorm_src 0
		.amdhsa_exception_fp_ieee_div_zero 0
		.amdhsa_exception_fp_ieee_overflow 0
		.amdhsa_exception_fp_ieee_underflow 0
		.amdhsa_exception_fp_ieee_inexact 0
		.amdhsa_exception_int_div_zero 0
	.end_amdhsa_kernel

.LBB2_132:
	s_load_dwordx8 s[4:11], s[0:1], 0x0
	s_load_dwordx2 s[34:35], s[0:1], 0x28
	s_load_dwordx2 s[12:13], s[0:1], 0x20
	v_lshl_or_b32 v34, s2, 14, v0
	s_waitcnt lgkmcnt(0)
	s_mov_b32 s14, 0x61a80
	s_mov_b32 s15, 0xf4240
	s_mov_b32 s16, 0x155cc0
	v_mov_b32_e32 v19, s4
	v_mov_b32_e32 v21, s5
	v_mov_b32_e32 v23, s6
	v_mov_b32_e32 v25, s7
	v_mov_b32_e32 v27, s8
	v_mov_b32_e32 v29, s9
	v_mov_b32_e32 v49, 0
	v_mov_b32_e32 v53, 0
	v_mov_b32_e32 v36, 0x30d40
	v_mov_b32_e32 v38, 0xfff6d840
	v_mov_b32_e32 v32, 0x61a80
	v_mov_b32_e32 v40, 0x61a80
	v_mov_b32_e32 v42, 0xf4240
	v_mov_b32_e32 v44, 0x30d40
	v_mov_b32_e32 v46, 0x61a80
	v_cmp_gt_u32_e64 s[18:19], s14, v34
	v_cmp_gt_u32_e64 s[20:21], s15, v34
	v_cmp_gt_u32_e64 s[22:23], s16, v34
	s_nop 0
	v_cndmask_b32_e64 v50, v27, v23, s[20:21]
	v_cndmask_b32_e64 v50, v50, v19, s[18:19]
	v_cndmask_b32_e64 v51, v29, v25, s[20:21]
	v_cndmask_b32_e64 v51, v51, v21, s[18:19]
	v_cndmask_b32_e64 v48, v38, v36, s[20:21]
	v_cndmask_b32_e64 v48, v48, v32, s[18:19]
	v_add_u32_e32 v48, v48, v34
	v_cndmask_b32_e64 v48, 0, v48, s[22:23]
	v_lshl_add_u64 v[52:53], v[48:49], 2, v[50:51]
	global_load_dword v33, v[52:53], off
	v_cndmask_b32_e64 v48, v42, v40, s[20:21]
	v_cndmask_b32_e64 v48, v48, 0, s[18:19]
	v_sub_u32_e32 v48, v34, v48
	v_cndmask_b32_e64 v48, 0, v48, s[22:23]
	v_lshl_add_u64 v[52:53], v[48:49], 2, v[50:51]
	global_load_dword v2, v[52:53], off
	v_add_u32_e32 v31, 0x400, v34
	v_cmp_gt_u32_e64 s[18:19], s14, v31
	v_cmp_gt_u32_e64 s[20:21], s15, v31
	v_cmp_gt_u32_e64 s[22:23], s16, v31
	s_nop 0
	v_cndmask_b32_e64 v50, v27, v23, s[20:21]
	v_cndmask_b32_e64 v50, v50, v19, s[18:19]
	v_cndmask_b32_e64 v51, v29, v25, s[20:21]
	v_cndmask_b32_e64 v51, v51, v21, s[18:19]
	v_cndmask_b32_e64 v48, v38, v36, s[20:21]
	v_cndmask_b32_e64 v48, v48, v32, s[18:19]
	v_add_u32_e32 v48, v48, v31
	v_cndmask_b32_e64 v48, 0, v48, s[22:23]
	v_lshl_add_u64 v[52:53], v[48:49], 2, v[50:51]
	global_load_dword v35, v[52:53], off
	v_cndmask_b32_e64 v48, v42, v40, s[20:21]
	v_cndmask_b32_e64 v48, v48, 0, s[18:19]
	v_sub_u32_e32 v48, v31, v48
	v_cndmask_b32_e64 v48, 0, v48, s[22:23]
	v_lshl_add_u64 v[52:53], v[48:49], 2, v[50:51]
	global_load_dword v1, v[52:53], off
	v_add_u32_e32 v31, 0x800, v34
	v_cmp_gt_u32_e64 s[18:19], s14, v31
	v_cmp_gt_u32_e64 s[20:21], s15, v31
	v_cmp_gt_u32_e64 s[22:23], s16, v31
	s_nop 0
	v_cndmask_b32_e64 v50, v27, v23, s[20:21]
	v_cndmask_b32_e64 v50, v50, v19, s[18:19]
	v_cndmask_b32_e64 v51, v29, v25, s[20:21]
	v_cndmask_b32_e64 v51, v51, v21, s[18:19]
	v_cndmask_b32_e64 v48, v38, v36, s[20:21]
	v_cndmask_b32_e64 v48, v48, v32, s[18:19]
	v_add_u32_e32 v48, v48, v31
	v_cndmask_b32_e64 v48, 0, v48, s[22:23]
	v_lshl_add_u64 v[52:53], v[48:49], 2, v[50:51]
	global_load_dword v6, v[52:53], off
	v_cndmask_b32_e64 v48, v42, v40, s[20:21]
	v_cndmask_b32_e64 v48, v48, 0, s[18:19]
	v_sub_u32_e32 v48, v31, v48
	v_cndmask_b32_e64 v48, 0, v48, s[22:23]
	v_lshl_add_u64 v[52:53], v[48:49], 2, v[50:51]
	global_load_dword v4, v[52:53], off
	v_add_u32_e32 v31, 0xc00, v34
	v_cmp_gt_u32_e64 s[18:19], s14, v31
	v_cmp_gt_u32_e64 s[20:21], s15, v31
	v_cmp_gt_u32_e64 s[22:23], s16, v31
	s_nop 0
	v_cndmask_b32_e64 v50, v27, v23, s[20:21]
	v_cndmask_b32_e64 v50, v50, v19, s[18:19]
	v_cndmask_b32_e64 v51, v29, v25, s[20:21]
	v_cndmask_b32_e64 v51, v51, v21, s[18:19]
	v_cndmask_b32_e64 v48, v38, v36, s[20:21]
	v_cndmask_b32_e64 v48, v48, v32, s[18:19]
	v_add_u32_e32 v48, v48, v31
	v_cndmask_b32_e64 v48, 0, v48, s[22:23]
	v_lshl_add_u64 v[52:53], v[48:49], 2, v[50:51]
	global_load_dword v37, v[52:53], off
	v_cndmask_b32_e64 v48, v42, v40, s[20:21]
	v_cndmask_b32_e64 v48, v48, 0, s[18:19]
	v_sub_u32_e32 v48, v31, v48
	v_cndmask_b32_e64 v48, 0, v48, s[22:23]
	v_lshl_add_u64 v[52:53], v[48:49], 2, v[50:51]
	global_load_dword v3, v[52:53], off
	v_add_u32_e32 v31, 0x1000, v34
	v_cmp_gt_u32_e64 s[18:19], s14, v31
	v_cmp_gt_u32_e64 s[20:21], s15, v31
	v_cmp_gt_u32_e64 s[22:23], s16, v31
	s_nop 0
	v_cndmask_b32_e64 v50, v27, v23, s[20:21]
	v_cndmask_b32_e64 v50, v50, v19, s[18:19]
	v_cndmask_b32_e64 v51, v29, v25, s[20:21]
	v_cndmask_b32_e64 v51, v51, v21, s[18:19]
	v_cndmask_b32_e64 v48, v38, v36, s[20:21]
	v_cndmask_b32_e64 v48, v48, v32, s[18:19]
	v_add_u32_e32 v48, v48, v31
	v_cndmask_b32_e64 v48, 0, v48, s[22:23]
	v_lshl_add_u64 v[52:53], v[48:49], 2, v[50:51]
	global_load_dword v10, v[52:53], off
	v_cndmask_b32_e64 v48, v42, v40, s[20:21]
	v_cndmask_b32_e64 v48, v48, 0, s[18:19]
	v_sub_u32_e32 v48, v31, v48
	v_cndmask_b32_e64 v48, 0, v48, s[22:23]
	v_lshl_add_u64 v[52:53], v[48:49], 2, v[50:51]
	global_load_dword v8, v[52:53], off
	v_add_u32_e32 v31, 0x1400, v34
	v_cmp_gt_u32_e64 s[18:19], s14, v31
	v_cmp_gt_u32_e64 s[20:21], s15, v31
	v_cmp_gt_u32_e64 s[22:23], s16, v31
	s_nop 0
	v_cndmask_b32_e64 v50, v27, v23, s[20:21]
	v_cndmask_b32_e64 v50, v50, v19, s[18:19]
	v_cndmask_b32_e64 v51, v29, v25, s[20:21]
	v_cndmask_b32_e64 v51, v51, v21, s[18:19]
	v_cndmask_b32_e64 v48, v38, v36, s[20:21]
	v_cndmask_b32_e64 v48, v48, v32, s[18:19]
	v_add_u32_e32 v48, v48, v31
	v_cndmask_b32_e64 v48, 0, v48, s[22:23]
	v_lshl_add_u64 v[52:53], v[48:49], 2, v[50:51]
	global_load_dword v39, v[52:53], off
	v_cndmask_b32_e64 v48, v42, v40, s[20:21]
	v_cndmask_b32_e64 v48, v48, 0, s[18:19]
	v_sub_u32_e32 v48, v31, v48
	v_cndmask_b32_e64 v48, 0, v48, s[22:23]
	v_lshl_add_u64 v[52:53], v[48:49], 2, v[50:51]
	global_load_dword v5, v[52:53], off
	v_add_u32_e32 v31, 0x1800, v34
	v_cmp_gt_u32_e64 s[18:19], s14, v31
	v_cmp_gt_u32_e64 s[20:21], s15, v31
	v_cmp_gt_u32_e64 s[22:23], s16, v31
	s_nop 0
	v_cndmask_b32_e64 v50, v27, v23, s[20:21]
	v_cndmask_b32_e64 v50, v50, v19, s[18:19]
	v_cndmask_b32_e64 v51, v29, v25, s[20:21]
	v_cndmask_b32_e64 v51, v51, v21, s[18:19]
	v_cndmask_b32_e64 v48, v38, v36, s[20:21]
	v_cndmask_b32_e64 v48, v48, v32, s[18:19]
	v_add_u32_e32 v48, v48, v31
	v_cndmask_b32_e64 v48, 0, v48, s[22:23]
	v_lshl_add_u64 v[52:53], v[48:49], 2, v[50:51]
	global_load_dword v14, v[52:53], off
	v_cndmask_b32_e64 v48, v42, v40, s[20:21]
	v_cndmask_b32_e64 v48, v48, 0, s[18:19]
	v_sub_u32_e32 v48, v31, v48
	v_cndmask_b32_e64 v48, 0, v48, s[22:23]
	v_lshl_add_u64 v[52:53], v[48:49], 2, v[50:51]
	global_load_dword v12, v[52:53], off
	v_add_u32_e32 v31, 0x1c00, v34
	v_cmp_gt_u32_e64 s[18:19], s14, v31
	v_cmp_gt_u32_e64 s[20:21], s15, v31
	v_cmp_gt_u32_e64 s[22:23], s16, v31
	s_nop 0
	v_cndmask_b32_e64 v50, v27, v23, s[20:21]
	v_cndmask_b32_e64 v50, v50, v19, s[18:19]
	v_cndmask_b32_e64 v51, v29, v25, s[20:21]
	v_cndmask_b32_e64 v51, v51, v21, s[18:19]
	v_cndmask_b32_e64 v48, v38, v36, s[20:21]
	v_cndmask_b32_e64 v48, v48, v32, s[18:19]
	v_add_u32_e32 v48, v48, v31
	v_cndmask_b32_e64 v48, 0, v48, s[22:23]
	v_lshl_add_u64 v[52:53], v[48:49], 2, v[50:51]
	global_load_dword v41, v[52:53], off
	v_cndmask_b32_e64 v48, v42, v40, s[20:21]
	v_cndmask_b32_e64 v48, v48, 0, s[18:19]
	v_sub_u32_e32 v48, v31, v48
	v_cndmask_b32_e64 v48, 0, v48, s[22:23]
	v_lshl_add_u64 v[52:53], v[48:49], 2, v[50:51]
	global_load_dword v7, v[52:53], off
	v_add_u32_e32 v31, 0x2000, v34
	v_cmp_gt_u32_e64 s[18:19], s14, v31
	v_cmp_gt_u32_e64 s[20:21], s15, v31
	v_cmp_gt_u32_e64 s[22:23], s16, v31
	s_nop 0
	v_cndmask_b32_e64 v50, v27, v23, s[20:21]
	v_cndmask_b32_e64 v50, v50, v19, s[18:19]
	v_cndmask_b32_e64 v51, v29, v25, s[20:21]
	v_cndmask_b32_e64 v51, v51, v21, s[18:19]
	v_cndmask_b32_e64 v48, v38, v36, s[20:21]
	v_cndmask_b32_e64 v48, v48, v32, s[18:19]
	v_add_u32_e32 v48, v48, v31
	v_cndmask_b32_e64 v48, 0, v48, s[22:23]
	v_lshl_add_u64 v[52:53], v[48:49], 2, v[50:51]
	global_load_dword v18, v[52:53], off
	v_cndmask_b32_e64 v48, v42, v40, s[20:21]
	v_cndmask_b32_e64 v48, v48, 0, s[18:19]
	v_sub_u32_e32 v48, v31, v48
	v_cndmask_b32_e64 v48, 0, v48, s[22:23]
	v_lshl_add_u64 v[52:53], v[48:49], 2, v[50:51]
	global_load_dword v16, v[52:53], off
	v_add_u32_e32 v31, 0x2400, v34
	v_cmp_gt_u32_e64 s[18:19], s14, v31
	v_cmp_gt_u32_e64 s[20:21], s15, v31
	v_cmp_gt_u32_e64 s[22:23], s16, v31
	s_nop 0
	v_cndmask_b32_e64 v50, v27, v23, s[20:21]
	v_cndmask_b32_e64 v50, v50, v19, s[18:19]
	v_cndmask_b32_e64 v51, v29, v25, s[20:21]
	v_cndmask_b32_e64 v51, v51, v21, s[18:19]
	v_cndmask_b32_e64 v48, v38, v36, s[20:21]
	v_cndmask_b32_e64 v48, v48, v32, s[18:19]
	v_add_u32_e32 v48, v48, v31
	v_cndmask_b32_e64 v48, 0, v48, s[22:23]
	v_lshl_add_u64 v[52:53], v[48:49], 2, v[50:51]
	global_load_dword v43, v[52:53], off
	v_cndmask_b32_e64 v48, v42, v40, s[20:21]
	v_cndmask_b32_e64 v48, v48, 0, s[18:19]
	v_sub_u32_e32 v48, v31, v48
	v_cndmask_b32_e64 v48, 0, v48, s[22:23]
	v_lshl_add_u64 v[52:53], v[48:49], 2, v[50:51]
	global_load_dword v9, v[52:53], off
	v_add_u32_e32 v31, 0x2800, v34
	v_cmp_gt_u32_e64 s[18:19], s14, v31
	v_cmp_gt_u32_e64 s[20:21], s15, v31
	v_cmp_gt_u32_e64 s[22:23], s16, v31
	s_nop 0
	v_cndmask_b32_e64 v50, v27, v23, s[20:21]
	v_cndmask_b32_e64 v50, v50, v19, s[18:19]
	v_cndmask_b32_e64 v51, v29, v25, s[20:21]
	v_cndmask_b32_e64 v51, v51, v21, s[18:19]
	v_cndmask_b32_e64 v48, v38, v36, s[20:21]
	v_cndmask_b32_e64 v48, v48, v32, s[18:19]
	v_add_u32_e32 v48, v48, v31
	v_cndmask_b32_e64 v48, 0, v48, s[22:23]
	v_lshl_add_u64 v[52:53], v[48:49], 2, v[50:51]
	global_load_dword v22, v[52:53], off
	v_cndmask_b32_e64 v48, v42, v40, s[20:21]
	v_cndmask_b32_e64 v48, v48, 0, s[18:19]
	v_sub_u32_e32 v48, v31, v48
	v_cndmask_b32_e64 v48, 0, v48, s[22:23]
	v_lshl_add_u64 v[52:53], v[48:49], 2, v[50:51]
	global_load_dword v20, v[52:53], off
	v_add_u32_e32 v31, 0x2c00, v34
	v_cmp_gt_u32_e64 s[18:19], s14, v31
	v_cmp_gt_u32_e64 s[20:21], s15, v31
	v_cmp_gt_u32_e64 s[22:23], s16, v31
	s_nop 0
	v_cndmask_b32_e64 v50, v27, v23, s[20:21]
	v_cndmask_b32_e64 v50, v50, v19, s[18:19]
	v_cndmask_b32_e64 v51, v29, v25, s[20:21]
	v_cndmask_b32_e64 v51, v51, v21, s[18:19]
	v_cndmask_b32_e64 v48, v38, v36, s[20:21]
	v_cndmask_b32_e64 v48, v48, v32, s[18:19]
	v_add_u32_e32 v48, v48, v31
	v_cndmask_b32_e64 v48, 0, v48, s[22:23]
	v_lshl_add_u64 v[52:53], v[48:49], 2, v[50:51]
	global_load_dword v45, v[52:53], off
	v_cndmask_b32_e64 v48, v42, v40, s[20:21]
	v_cndmask_b32_e64 v48, v48, 0, s[18:19]
	v_sub_u32_e32 v48, v31, v48
	v_cndmask_b32_e64 v48, 0, v48, s[22:23]
	v_lshl_add_u64 v[52:53], v[48:49], 2, v[50:51]
	global_load_dword v11, v[52:53], off
	v_add_u32_e32 v31, 0x3000, v34
	v_cmp_gt_u32_e64 s[18:19], s14, v31
	v_cmp_gt_u32_e64 s[20:21], s15, v31
	v_cmp_gt_u32_e64 s[22:23], s16, v31
	s_nop 0
	v_cndmask_b32_e64 v50, v27, v23, s[20:21]
	v_cndmask_b32_e64 v50, v50, v19, s[18:19]
	v_cndmask_b32_e64 v51, v29, v25, s[20:21]
	v_cndmask_b32_e64 v51, v51, v21, s[18:19]
	v_cndmask_b32_e64 v48, v38, v36, s[20:21]
	v_cndmask_b32_e64 v48, v48, v32, s[18:19]
	v_add_u32_e32 v48, v48, v31
	v_cndmask_b32_e64 v48, 0, v48, s[22:23]
	v_lshl_add_u64 v[52:53], v[48:49], 2, v[50:51]
	global_load_dword v26, v[52:53], off
	v_cndmask_b32_e64 v48, v42, v40, s[20:21]
	v_cndmask_b32_e64 v48, v48, 0, s[18:19]
	v_sub_u32_e32 v48, v31, v48
	v_cndmask_b32_e64 v48, 0, v48, s[22:23]
	v_lshl_add_u64 v[52:53], v[48:49], 2, v[50:51]
	global_load_dword v24, v[52:53], off
	v_add_u32_e32 v31, 0x3400, v34
	v_cmp_gt_u32_e64 s[18:19], s14, v31
	v_cmp_gt_u32_e64 s[20:21], s15, v31
	v_cmp_gt_u32_e64 s[22:23], s16, v31
	s_nop 0
	v_cndmask_b32_e64 v50, v27, v23, s[20:21]
	v_cndmask_b32_e64 v50, v50, v19, s[18:19]
	v_cndmask_b32_e64 v51, v29, v25, s[20:21]
	v_cndmask_b32_e64 v51, v51, v21, s[18:19]
	v_cndmask_b32_e64 v48, v38, v36, s[20:21]
	v_cndmask_b32_e64 v48, v48, v32, s[18:19]
	v_add_u32_e32 v48, v48, v31
	v_cndmask_b32_e64 v48, 0, v48, s[22:23]
	v_lshl_add_u64 v[52:53], v[48:49], 2, v[50:51]
	global_load_dword v47, v[52:53], off
	v_cndmask_b32_e64 v48, v42, v40, s[20:21]
	v_cndmask_b32_e64 v48, v48, 0, s[18:19]
	v_sub_u32_e32 v48, v31, v48
	v_cndmask_b32_e64 v48, 0, v48, s[22:23]
	v_lshl_add_u64 v[52:53], v[48:49], 2, v[50:51]
	global_load_dword v13, v[52:53], off
	v_add_u32_e32 v31, 0x3800, v34
	v_cmp_gt_u32_e64 s[18:19], s14, v31
	v_cmp_gt_u32_e64 s[20:21], s15, v31
	v_cmp_gt_u32_e64 s[22:23], s16, v31
	s_nop 0
	v_cndmask_b32_e64 v50, v27, v23, s[20:21]
	v_cndmask_b32_e64 v50, v50, v19, s[18:19]
	v_cndmask_b32_e64 v51, v29, v25, s[20:21]
	v_cndmask_b32_e64 v51, v51, v21, s[18:19]
	v_cndmask_b32_e64 v48, v38, v36, s[20:21]
	v_cndmask_b32_e64 v48, v48, v32, s[18:19]
	v_add_u32_e32 v48, v48, v31
	v_cndmask_b32_e64 v48, 0, v48, s[22:23]
	v_lshl_add_u64 v[52:53], v[48:49], 2, v[50:51]
	global_load_dword v30, v[52:53], off
	v_cndmask_b32_e64 v48, v42, v40, s[20:21]
	v_cndmask_b32_e64 v48, v48, 0, s[18:19]
	v_sub_u32_e32 v48, v31, v48
	v_cndmask_b32_e64 v48, 0, v48, s[22:23]
	v_lshl_add_u64 v[52:53], v[48:49], 2, v[50:51]
	global_load_dword v28, v[52:53], off
	v_add_u32_e32 v31, 0x3c00, v34
	v_cmp_gt_u32_e64 s[18:19], s14, v31
	v_cmp_gt_u32_e64 s[20:21], s15, v31
	v_cmp_gt_u32_e64 s[22:23], s16, v31
	s_nop 0
	v_cndmask_b32_e64 v50, v27, v23, s[20:21]
	v_cndmask_b32_e64 v50, v50, v19, s[18:19]
	v_cndmask_b32_e64 v51, v29, v25, s[20:21]
	v_cndmask_b32_e64 v51, v51, v21, s[18:19]
	v_cndmask_b32_e64 v48, v38, v36, s[20:21]
	v_cndmask_b32_e64 v48, v48, v32, s[18:19]
	v_add_u32_e32 v48, v48, v31
	v_cndmask_b32_e64 v48, 0, v48, s[22:23]
	v_lshl_add_u64 v[52:53], v[48:49], 2, v[50:51]
	global_load_dword v17, v[52:53], off
	v_cndmask_b32_e64 v48, v42, v40, s[20:21]
	v_cndmask_b32_e64 v48, v48, 0, s[18:19]
	v_sub_u32_e32 v48, v31, v48
	v_cndmask_b32_e64 v48, 0, v48, s[22:23]
	v_lshl_add_u64 v[52:53], v[48:49], 2, v[50:51]
	global_load_dword v15, v[52:53], off
	s_waitcnt vmcnt(0)
	v_mov_b32_e32 v50, -1
	v_cmp_gt_u32_e64 s[18:19], s14, v34
	v_cmp_gt_u32_e64 s[20:21], s15, v34
	v_cmp_gt_u32_e64 s[22:23], s16, v34
	s_nop 0
	v_cndmask_b32_e64 v48, v46, v44, s[20:21]
	v_cndmask_b32_e64 v48, v48, 0, s[18:19]
	v_add_u32_e32 v33, v33, v48
	v_cndmask_b32_e64 v33, v50, v33, s[22:23]
	v_cndmask_b32_e64 v2, 0, v2, s[22:23]
	v_add_u32_e32 v31, 0x400, v34
	v_cmp_gt_u32_e64 s[18:19], s14, v31
	v_cmp_gt_u32_e64 s[20:21], s15, v31
	v_cmp_gt_u32_e64 s[22:23], s16, v31
	s_nop 0
	v_cndmask_b32_e64 v48, v46, v44, s[20:21]
	v_cndmask_b32_e64 v48, v48, 0, s[18:19]
	v_add_u32_e32 v35, v35, v48
	v_cndmask_b32_e64 v35, v50, v35, s[22:23]
	v_cndmask_b32_e64 v1, 0, v1, s[22:23]
	v_add_u32_e32 v31, 0x800, v34
	v_cmp_gt_u32_e64 s[18:19], s14, v31
	v_cmp_gt_u32_e64 s[20:21], s15, v31
	v_cmp_gt_u32_e64 s[22:23], s16, v31
	s_nop 0
	v_cndmask_b32_e64 v48, v46, v44, s[20:21]
	v_cndmask_b32_e64 v48, v48, 0, s[18:19]
	v_add_u32_e32 v6, v6, v48
	v_cndmask_b32_e64 v6, v50, v6, s[22:23]
	v_cndmask_b32_e64 v4, 0, v4, s[22:23]
	v_add_u32_e32 v31, 0xc00, v34
	v_cmp_gt_u32_e64 s[18:19], s14, v31
	v_cmp_gt_u32_e64 s[20:21], s15, v31
	v_cmp_gt_u32_e64 s[22:23], s16, v31
	s_nop 0
	v_cndmask_b32_e64 v48, v46, v44, s[20:21]
	v_cndmask_b32_e64 v48, v48, 0, s[18:19]
	v_add_u32_e32 v37, v37, v48
	v_cndmask_b32_e64 v37, v50, v37, s[22:23]
	v_cndmask_b32_e64 v3, 0, v3, s[22:23]
	v_add_u32_e32 v31, 0x1000, v34
	v_cmp_gt_u32_e64 s[18:19], s14, v31
	v_cmp_gt_u32_e64 s[20:21], s15, v31
	v_cmp_gt_u32_e64 s[22:23], s16, v31
	s_nop 0
	v_cndmask_b32_e64 v48, v46, v44, s[20:21]
	v_cndmask_b32_e64 v48, v48, 0, s[18:19]
	v_add_u32_e32 v10, v10, v48
	v_cndmask_b32_e64 v10, v50, v10, s[22:23]
	v_cndmask_b32_e64 v8, 0, v8, s[22:23]
	v_add_u32_e32 v31, 0x1400, v34
	v_cmp_gt_u32_e64 s[18:19], s14, v31
	v_cmp_gt_u32_e64 s[20:21], s15, v31
	v_cmp_gt_u32_e64 s[22:23], s16, v31
	s_nop 0
	v_cndmask_b32_e64 v48, v46, v44, s[20:21]
	v_cndmask_b32_e64 v48, v48, 0, s[18:19]
	v_add_u32_e32 v39, v39, v48
	v_cndmask_b32_e64 v39, v50, v39, s[22:23]
	v_cndmask_b32_e64 v5, 0, v5, s[22:23]
	v_add_u32_e32 v31, 0x1800, v34
	v_cmp_gt_u32_e64 s[18:19], s14, v31
	v_cmp_gt_u32_e64 s[20:21], s15, v31
	v_cmp_gt_u32_e64 s[22:23], s16, v31
	s_nop 0
	v_cndmask_b32_e64 v48, v46, v44, s[20:21]
	v_cndmask_b32_e64 v48, v48, 0, s[18:19]
	v_add_u32_e32 v14, v14, v48
	v_cndmask_b32_e64 v14, v50, v14, s[22:23]
	v_cndmask_b32_e64 v12, 0, v12, s[22:23]
	v_add_u32_e32 v31, 0x1c00, v34
	v_cmp_gt_u32_e64 s[18:19], s14, v31
	v_cmp_gt_u32_e64 s[20:21], s15, v31
	v_cmp_gt_u32_e64 s[22:23], s16, v31
	s_nop 0
	v_cndmask_b32_e64 v48, v46, v44, s[20:21]
	v_cndmask_b32_e64 v48, v48, 0, s[18:19]
	v_add_u32_e32 v41, v41, v48
	v_cndmask_b32_e64 v41, v50, v41, s[22:23]
	v_cndmask_b32_e64 v7, 0, v7, s[22:23]
	v_add_u32_e32 v31, 0x2000, v34
	v_cmp_gt_u32_e64 s[18:19], s14, v31
	v_cmp_gt_u32_e64 s[20:21], s15, v31
	v_cmp_gt_u32_e64 s[22:23], s16, v31
	s_nop 0
	v_cndmask_b32_e64 v48, v46, v44, s[20:21]
	v_cndmask_b32_e64 v48, v48, 0, s[18:19]
	v_add_u32_e32 v18, v18, v48
	v_cndmask_b32_e64 v18, v50, v18, s[22:23]
	v_cndmask_b32_e64 v16, 0, v16, s[22:23]
	v_add_u32_e32 v31, 0x2400, v34
	v_cmp_gt_u32_e64 s[18:19], s14, v31
	v_cmp_gt_u32_e64 s[20:21], s15, v31
	v_cmp_gt_u32_e64 s[22:23], s16, v31
	s_nop 0
	v_cndmask_b32_e64 v48, v46, v44, s[20:21]
	v_cndmask_b32_e64 v48, v48, 0, s[18:19]
	v_add_u32_e32 v43, v43, v48
	v_cndmask_b32_e64 v43, v50, v43, s[22:23]
	v_cndmask_b32_e64 v9, 0, v9, s[22:23]
	v_add_u32_e32 v31, 0x2800, v34
	v_cmp_gt_u32_e64 s[18:19], s14, v31
	v_cmp_gt_u32_e64 s[20:21], s15, v31
	v_cmp_gt_u32_e64 s[22:23], s16, v31
	s_nop 0
	v_cndmask_b32_e64 v48, v46, v44, s[20:21]
	v_cndmask_b32_e64 v48, v48, 0, s[18:19]
	v_add_u32_e32 v22, v22, v48
	v_cndmask_b32_e64 v22, v50, v22, s[22:23]
	v_cndmask_b32_e64 v20, 0, v20, s[22:23]
	v_add_u32_e32 v31, 0x2c00, v34
	v_cmp_gt_u32_e64 s[18:19], s14, v31
	v_cmp_gt_u32_e64 s[20:21], s15, v31
	v_cmp_gt_u32_e64 s[22:23], s16, v31
	s_nop 0
	v_cndmask_b32_e64 v48, v46, v44, s[20:21]
	v_cndmask_b32_e64 v48, v48, 0, s[18:19]
	v_add_u32_e32 v45, v45, v48
	v_cndmask_b32_e64 v45, v50, v45, s[22:23]
	v_cndmask_b32_e64 v11, 0, v11, s[22:23]
	v_add_u32_e32 v31, 0x3000, v34
	v_cmp_gt_u32_e64 s[18:19], s14, v31
	v_cmp_gt_u32_e64 s[20:21], s15, v31
	v_cmp_gt_u32_e64 s[22:23], s16, v31
	s_nop 0
	v_cndmask_b32_e64 v48, v46, v44, s[20:21]
	v_cndmask_b32_e64 v48, v48, 0, s[18:19]
	v_add_u32_e32 v26, v26, v48
	v_cndmask_b32_e64 v26, v50, v26, s[22:23]
	v_cndmask_b32_e64 v24, 0, v24, s[22:23]
	v_add_u32_e32 v31, 0x3400, v34
	v_cmp_gt_u32_e64 s[18:19], s14, v31
	v_cmp_gt_u32_e64 s[20:21], s15, v31
	v_cmp_gt_u32_e64 s[22:23], s16, v31
	s_nop 0
	v_cndmask_b32_e64 v48, v46, v44, s[20:21]
	v_cndmask_b32_e64 v48, v48, 0, s[18:19]
	v_add_u32_e32 v47, v47, v48
	v_cndmask_b32_e64 v47, v50, v47, s[22:23]
	v_cndmask_b32_e64 v13, 0, v13, s[22:23]
	v_add_u32_e32 v31, 0x3800, v34
	v_cmp_gt_u32_e64 s[18:19], s14, v31
	v_cmp_gt_u32_e64 s[20:21], s15, v31
	v_cmp_gt_u32_e64 s[22:23], s16, v31
	s_nop 0
	v_cndmask_b32_e64 v48, v46, v44, s[20:21]
	v_cndmask_b32_e64 v48, v48, 0, s[18:19]
	v_add_u32_e32 v30, v30, v48
	v_cndmask_b32_e64 v30, v50, v30, s[22:23]
	v_cndmask_b32_e64 v28, 0, v28, s[22:23]
	v_add_u32_e32 v31, 0x3c00, v34
	v_cmp_gt_u32_e64 s[18:19], s14, v31
	v_cmp_gt_u32_e64 s[20:21], s15, v31
	v_cmp_gt_u32_e64 s[22:23], s16, v31
	s_nop 0
	v_cndmask_b32_e64 v48, v46, v44, s[20:21]
	v_cndmask_b32_e64 v48, v48, 0, s[18:19]
	v_add_u32_e32 v17, v17, v48
	v_cndmask_b32_e64 v17, v50, v17, s[22:23]
	v_cndmask_b32_e64 v15, 0, v15, s[22:23]
	s_mov_b64 s[0:1], exec

_Z12k_layer_pool9LayerArgs:
	s_load_dwordx8 s[4:11], s[0:1], 0x0
	s_load_dwordx8 s[12:19], s[0:1], 0x20
	s_load_dwordx2 s[22:23], s[0:1], 0x60
	s_load_dwordx2 s[30:31], s[0:1], 0x58
	v_and_b32_e32 v159, 63, v0
	v_lshrrev_b32_e32 v160, 6, v0
	v_and_b32_e32 v143, 3, v159
	v_and_b32_e32 v167, 15, v159
	s_nop 0
	v_readfirstlane_b32 s61, v160
	s_waitcnt lgkmcnt(0)
	s_mov_b64 s[26:27], s[6:7]
	s_mov_b64 s[28:29], s[10:11]
	s_mov_b64 s[24:25], s[14:15]
	s_mov_b64 s[64:65], s[16:17]
	s_mov_b64 s[66:67], s[18:19]
	s_mov_b64 s[68:69], s[8:9]
	s_mov_b32 s8, s4
	s_and_b32 s9, s5, 0xffff
	s_mov_b32 s10, 0x40000000
	s_mov_b32 s11, 0x20000
	s_mov_b32 s12, s68
	s_and_b32 s13, s69, 0xffff
	s_mov_b32 s14, 0x40000000
	s_mov_b32 s15, 0x20000
	s_add_u32 s16, s24, 0x712bd00
	s_addc_u32 s17, s25, 0
	s_add_u32 s18, s16, 0xc35000
	s_addc_u32 s19, s17, 0
	s_add_u32 s20, s16, 0x186a000
	s_addc_u32 s21, s17, 0
	s_mul_i32 s52, s2, 49
	s_mov_b32 s71, s52
	s_add_u32 s32, s52, 49
	s_min_u32 s32, s32, 12500
	s_add_u32 s35, s52, s61
	s_mul_i32 s61, s61, 0x1100
	s_add_u32 s61, s61, 0x18000
	v_lshrrev_b32_e32 v160, 2, v159
	v_lshrrev_b32_e32 v161, 4, v159
	v_lshlrev_b32_e32 v134, 4, v143
	v_mov_b32_e32 v135, v134
	v_mul_u32_u24_e32 v162, 0x110, v160
	v_add3_u32 v136, v162, v134, s61
	v_mul_u32_u24_e32 v162, 0x110, v167
	v_lshl_add_u32 v137, v161, 4, v162
	v_add_u32_e32 v137, s61, v137
	v_lshl_add_u32 v140, v161, 3, v162
	v_add_u32_e32 v140, s61, v140
	v_mul_u32_u24_e32 v162, 0x110, v161
	v_lshl_add_u32 v141, v167, 4, v162
	v_add_u32_e32 v141, s61, v141
	v_lshlrev_b32_e32 v138, 4, v159
	v_add_u32_e32 v139, 0x10000, v138
	v_lshlrev_b32_e32 v142, 8, v161
	v_lshl_add_u32 v142, v167, 4, v142
	v_mov_b32_e32 v144, 0x800000
	v_lshlrev_b32_e32 v145, 2, v160
	v_lshl_add_u32 v145, v143, 6, v145
	v_mul_u32_u24_e32 v146, 0x100, v160
	v_add_u32_e32 v146, v146, v135
	s_lshl_b32 s52, s35, 10
	v_add_u32_e32 v160, s52, v145
	global_load_dword v151, v160, s[16:17]
	global_load_dword v152, v160, s[16:17] offset:256
	global_load_dword v153, v160, s[18:19]
	global_load_dword v154, v160, s[18:19] offset:256
	s_lshl_b32 s52, s35, 2
	v_and_b32_e32 v161, 1, v159
	v_mul_u32_u24_e32 v161, 0xc350, v161
	v_add_u32_e32 v161, s52, v161
	global_load_dword v155, v161, s[20:21]
	s_min_u32 s52, s35, 12499
	s_lshl_b32 s52, s52, 6
	v_lshl_add_u32 v161, v167, 2, s52
	global_load_dword v164, v161, s[30:31]
	s_mov_b32 s40, s64
	s_and_b32 s41, s65, 0xffff
	s_mov_b32 s42, 0x18000
	s_mov_b32 s43, 0x20000
	v_lshlrev_b32_e32 v160, 4, v0
	buffer_load_dwordx4 v[2:5], v160, s[40:43], 0 offen
	v_add_u32_e32 v161, 0x3000, v160
	buffer_load_dwordx4 v[6:9], v161, s[40:43], 0 offen
	v_add_u32_e32 v161, 0x6000, v160
	buffer_load_dwordx4 v[10:13], v161, s[40:43], 0 offen
	v_add_u32_e32 v161, 0x9000, v160
	buffer_load_dwordx4 v[14:17], v161, s[40:43], 0 offen
	v_add_u32_e32 v161, 0xc000, v160
	buffer_load_dwordx4 v[18:21], v161, s[40:43], 0 offen
	v_add_u32_e32 v161, 0xf000, v160
	buffer_load_dwordx4 v[22:25], v161, s[40:43], 0 offen
	v_add_u32_e32 v161, 0x12000, v160
	buffer_load_dwordx4 v[26:29], v161, s[40:43], 0 offen
	v_add_u32_e32 v161, 0x15000, v160
	buffer_load_dwordx4 v[30:33], v161, s[40:43], 0 offen
	v_lshlrev_b32_e32 v162, 2, v0
	v_cmp_gt_u32_e32 vcc, 0x80, v0
	s_and_saveexec_b64 s[58:59], vcc
	s_cbranch_execz .Lfp_nobias
	global_load_dword v163, v162, s[66:67]
.Lfp_nobias:
	s_mov_b64 exec, s[58:59]
	v_mov_b32_e32 v157, 0
	v_add_u32_e32 v158, 0x24e00, v162
	ds_write_b32 v158, v157
	v_cmp_gt_u32_e32 vcc, 0x100, v0
	s_and_saveexec_b64 s[58:59], vcc
	ds_write_b32 v158, v157 offset:3072
	s_mov_b64 exec, s[58:59]
	s_lshl_b32 s53, s71, 6
	s_load_dword s60, s[30:31], s53
	s_waitcnt vmcnt(7)
	ds_write_b128 v160, v[2:5]
	s_waitcnt vmcnt(6)
	v_add_u32_e32 v161, 0x3000, v160
	ds_write_b128 v161, v[6:9]
	s_waitcnt vmcnt(5)
	v_add_u32_e32 v161, 0x6000, v160
	ds_write_b128 v161, v[10:13]
	s_waitcnt vmcnt(4)
	v_add_u32_e32 v161, 0x9000, v160
	ds_write_b128 v161, v[14:17]
	s_waitcnt vmcnt(3)
	v_add_u32_e32 v161, 0xc000, v160
	ds_write_b128 v161, v[18:21]
	s_waitcnt vmcnt(2)
	v_add_u32_e32 v161, 0xf000, v160
	ds_write_b128 v161, v[22:25]
	s_waitcnt vmcnt(1)
	v_add_u32_e32 v161, 0x12000, v160
	ds_write_b128 v161, v[26:29]
	s_waitcnt vmcnt(0)
	v_add_u32_e32 v161, 0x15000, v160
	ds_write_b128 v161, v[30:33]
	s_waitcnt vmcnt(0)
	v_cmp_gt_u32_e32 vcc, 0x80, v0
	s_and_saveexec_b64 s[58:59], vcc
	v_add_u32_e32 v162, 0x24c00, v162
	ds_write_b32 v162, v163
	s_mov_b64 exec, s[58:59]
	v_cmp_eq_u32_e32 vcc, 0, v0
	s_and_saveexec_b64 s[58:59], vcc
	v_mov_b32_e32 v160, 0x25e00
	s_add_u32 s53, s71, 12
	v_mov_b32_e32 v161, s53
	ds_write_b32 v160, v161
	s_mov_b64 exec, s[58:59]
	s_waitcnt lgkmcnt(0)
	s_barrier
	s_waitcnt vmcnt(0)
	s_mov_b32 s34, s35
	v_readlane_b32 s52, v155, 0
	v_readlane_b32 s53, v155, 1
	s_cmp_lt_u32 s34, s32
	s_cselect_b32 s47, s52, 0
	s_cselect_b32 s48, s53, 0
	s_max_u32 s38, s47, 2
	s_max_u32 s39, s48, 2
	v_cmp_gt_i32_e32 vcc, s47, v143
	s_nop 1
	v_cndmask_b32_e32 v147, v144, v151, vcc
	v_mov_b32_e32 v148, v152
	v_mov_b32_e32 v149, v153
	v_mov_b32_e32 v150, v154
	v_mov_b32_e32 v165, v164
	s_mov_b32 s44, 0
	s_mov_b32 s46, 0
	s_mov_b32 s45, s38
	s_mov_b64 s[40:41], s[8:9]
	s_mov_b64 s[42:43], s[10:11]
	s_movk_i32 s49, 0x100
	s_mov_b32 s70, 0
	v_mov_b32_e32 v160, 1
	v_mov_b32_e32 v161, 0x25e00
	s_mov_b64 s[58:59], exec
	s_mov_b64 exec, 1
	ds_add_rtn_u32 v160, v161, v160
	s_waitcnt lgkmcnt(0)
	v_readfirstlane_b32 s35, v160
	s_mov_b64 exec, s[58:59]
	s_lshl_b32 s52, s35, 10
	v_add_u32_e32 v160, s52, v145
	global_load_dword v151, v160, s[16:17]
	global_load_dword v152, v160, s[16:17] offset:256
	global_load_dword v153, v160, s[18:19]
	global_load_dword v154, v160, s[18:19] offset:256
	s_lshl_b32 s52, s35, 2
	v_and_b32_e32 v161, 1, v159
	v_mul_u32_u24_e32 v161, 0xc350, v161
	v_add_u32_e32 v161, s52, v161
	global_load_dword v155, v161, s[20:21]
	s_min_u32 s52, s35, 12499
	s_lshl_b32 s52, s52, 6
	v_lshl_add_u32 v161, v167, 2, s52
	global_load_dword v164, v161, s[30:31]
	s_waitcnt lgkmcnt(0)
	s_mov_b32 s64, 2
	s_mov_b32 s66, 0

_Z10k_layer_fhILi96ELb1EEv9LayerArgsS0_i:
	s_movk_i32 s3, 0x58
	v_lshrrev_b32_e32 v133, 6, v0
	s_movk_i32 s4, 0x1100
	v_mov_b32_e32 v1, 0x18000
	v_mad_u32_u24 v1, v133, s4, v1
	s_mov_b64 s[4:5], -1
	s_waitcnt lgkmcnt(0)
	s_cmp_ge_i32 s2, s3
	v_lshlrev_b32_e32 v130, 4, v0
	s_cbranch_scc0 .LBB5_73
	s_load_dwordx8 s[4:11], s[0:1], 0x0
	s_load_dwordx8 s[12:19], s[0:1], 0x20
	s_load_dwordx2 s[22:23], s[0:1], 0x40
	v_and_b32_e32 v159, 63, v0
	v_lshrrev_b32_e32 v160, 6, v0
	v_and_b32_e32 v143, 3, v159
	v_and_b32_e32 v167, 15, v159
	s_nop 0
	v_readfirstlane_b32 s61, v160
	s_waitcnt lgkmcnt(0)
	s_mov_b64 s[26:27], s[6:7]
	s_mov_b64 s[28:29], s[10:11]
	s_mov_b64 s[24:25], s[14:15]
	s_mov_b64 s[64:65], s[16:17]
	s_mov_b64 s[66:67], s[18:19]
	s_mov_b64 s[68:69], s[8:9]
	s_mov_b32 s8, s4
	s_and_b32 s9, s5, 0xffff
	s_mov_b32 s10, 0x40000000
	s_mov_b32 s11, 0x20000
	s_mov_b32 s12, s68
	s_and_b32 s13, s69, 0xffff
	s_mov_b32 s14, 0x40000000
	s_mov_b32 s15, 0x20000
	s_add_u32 s16, s24, 0x712bd00
	s_addc_u32 s17, s25, 0
	s_add_u32 s18, s16, 0xc35000
	s_addc_u32 s19, s17, 0
	s_add_u32 s20, s16, 0x186a000
	s_addc_u32 s21, s17, 0
	s_sub_u32 s52, s2, 88
	s_mul_i32 s52, s52, 75
	s_mov_b32 s71, s52
	s_add_u32 s32, s52, 75
	s_min_u32 s32, s32, 12500
	s_add_u32 s35, s52, s61
	s_mul_i32 s61, s61, 0x1100
	s_add_u32 s61, s61, 0x18000
	v_lshrrev_b32_e32 v160, 2, v159
	v_lshrrev_b32_e32 v161, 4, v159
	v_lshlrev_b32_e32 v134, 4, v143
	v_mov_b32_e32 v135, v134
	v_mul_u32_u24_e32 v162, 0x110, v160
	v_add3_u32 v136, v162, v134, s61
	v_mul_u32_u24_e32 v162, 0x110, v167
	v_lshl_add_u32 v137, v161, 4, v162
	v_add_u32_e32 v137, s61, v137
	v_lshl_add_u32 v140, v161, 3, v162
	v_add_u32_e32 v140, s61, v140
	v_mul_u32_u24_e32 v162, 0x110, v161
	v_lshl_add_u32 v141, v167, 4, v162
	v_add_u32_e32 v141, s61, v141
	v_lshlrev_b32_e32 v138, 4, v159
	v_add_u32_e32 v139, 0x10000, v138
	v_lshlrev_b32_e32 v142, 8, v161
	v_lshl_add_u32 v142, v167, 4, v142
	v_mov_b32_e32 v144, 0x800000
	v_lshlrev_b32_e32 v145, 2, v160
	v_lshl_add_u32 v145, v143, 6, v145
	v_mul_u32_u24_e32 v146, 0xc0, v160
	v_add_u32_e32 v146, v146, v135
	s_lshl_b32 s52, s35, 10
	v_add_u32_e32 v160, s52, v145
	global_load_dword v151, v160, s[16:17]
	global_load_dword v152, v160, s[16:17] offset:256
	global_load_dword v153, v160, s[18:19]
	global_load_dword v154, v160, s[18:19] offset:256
	s_lshl_b32 s52, s35, 2
	v_and_b32_e32 v161, 1, v159
	v_mul_u32_u24_e32 v161, 0xc350, v161
	v_add_u32_e32 v161, s52, v161
	global_load_dword v155, v161, s[20:21]
	s_mov_b32 s40, s64
	s_and_b32 s41, s65, 0xffff
	s_mov_b32 s42, 0x14000
	s_mov_b32 s43, 0x20000
	v_lshlrev_b32_e32 v160, 4, v0
	buffer_load_dwordx4 v[2:5], v160, s[40:43], 0 offen
	v_add_u32_e32 v161, 0x3000, v160
	buffer_load_dwordx4 v[6:9], v161, s[40:43], 0 offen
	v_add_u32_e32 v161, 0x6000, v160
	buffer_load_dwordx4 v[10:13], v161, s[40:43], 0 offen
	v_add_u32_e32 v161, 0x9000, v160
	buffer_load_dwordx4 v[14:17], v161, s[40:43], 0 offen
	v_add_u32_e32 v161, 0xc000, v160
	buffer_load_dwordx4 v[18:21], v161, s[40:43], 0 offen
	v_add_u32_e32 v161, 0xf000, v160
	buffer_load_dwordx4 v[22:25], v161, s[40:43], 0 offen
	v_add_u32_e32 v161, 0x12000, v160
	buffer_load_dwordx4 v[26:29], v161, s[40:43], 0 offen
	v_lshlrev_b32_e32 v162, 2, v0
	v_cmp_gt_u32_e32 vcc, 0x80, v0
	s_and_saveexec_b64 s[58:59], vcc
	s_cbranch_execz .Lfa_nobias
	global_load_dword v163, v162, s[66:67]
.Lfa_nobias:
	s_mov_b64 exec, s[58:59]
	s_waitcnt vmcnt(6)
	ds_write_b128 v160, v[2:5]
	s_waitcnt vmcnt(5)
	v_add_u32_e32 v161, 0x3000, v160
	ds_write_b128 v161, v[6:9]
	s_waitcnt vmcnt(4)
	v_add_u32_e32 v161, 0x6000, v160
	ds_write_b128 v161, v[10:13]
	s_waitcnt vmcnt(3)
	v_add_u32_e32 v161, 0x9000, v160
	ds_write_b128 v161, v[14:17]
	s_waitcnt vmcnt(2)
	v_add_u32_e32 v161, 0xc000, v160
	ds_write_b128 v161, v[18:21]
	s_waitcnt vmcnt(1)
	v_add_u32_e32 v161, 0xf000, v160
	ds_write_b128 v161, v[22:25]
	s_waitcnt vmcnt(0)
	v_add_u32_e32 v161, 0x12000, v160
	ds_write_b128 v161, v[26:29]
	s_waitcnt vmcnt(0)
	v_cmp_gt_u32_e32 vcc, 0x80, v0
	s_and_saveexec_b64 s[58:59], vcc
	v_add_u32_e32 v162, 0x24c00, v162
	ds_write_b32 v162, v163
	s_mov_b64 exec, s[58:59]
	v_cmp_eq_u32_e32 vcc, 0, v0
	s_and_saveexec_b64 s[58:59], vcc
	v_mov_b32_e32 v160, 0x24e00
	s_add_u32 s53, s71, 12
	v_mov_b32_e32 v161, s53
	ds_write_b32 v160, v161
	s_mov_b64 exec, s[58:59]
	s_waitcnt lgkmcnt(0)
	s_barrier
	s_waitcnt vmcnt(0)
	s_mov_b32 s34, s35
	v_readlane_b32 s52, v155, 0
	v_readlane_b32 s53, v155, 1
	s_cmp_lt_u32 s34, s32
	s_cselect_b32 s47, s52, 0
	s_cselect_b32 s48, s53, 0
	s_max_u32 s38, s47, 2
	s_max_u32 s39, s48, 2
	v_cmp_gt_i32_e32 vcc, s47, v143
	s_nop 1
	v_cndmask_b32_e32 v147, v144, v151, vcc
	v_mov_b32_e32 v148, v152
	v_mov_b32_e32 v149, v153
	v_mov_b32_e32 v150, v154
	s_mov_b32 s44, 0
	s_mov_b32 s46, 0
	s_mov_b32 s45, s38
	s_mov_b64 s[40:41], s[8:9]
	s_mov_b64 s[42:43], s[10:11]
	s_movk_i32 s49, 0x100
	s_mov_b32 s70, 0
	v_mov_b32_e32 v160, 1
	v_mov_b32_e32 v161, 0x24e00
	s_mov_b64 s[58:59], exec
	s_mov_b64 exec, 1
	ds_add_rtn_u32 v160, v161, v160
	s_waitcnt lgkmcnt(0)
	v_readfirstlane_b32 s35, v160
	s_mov_b64 exec, s[58:59]
	s_lshl_b32 s52, s35, 10
	v_add_u32_e32 v160, s52, v145
	global_load_dword v151, v160, s[16:17]
	global_load_dword v152, v160, s[16:17] offset:256
	global_load_dword v153, v160, s[18:19]
	global_load_dword v154, v160, s[18:19] offset:256
	s_lshl_b32 s52, s35, 2
	v_and_b32_e32 v161, 1, v159
	v_mul_u32_u24_e32 v161, 0xc350, v161
	v_add_u32_e32 v161, s52, v161
	global_load_dword v155, v161, s[20:21]
	s_mov_b32 s64, 2
	s_mov_b32 s66, 0

_Z10k_layer_fhILi128ELb1EEv9LayerArgsS0_i:
	s_movk_i32 s3, 0x58
	v_lshrrev_b32_e32 v138, 6, v0
	s_movk_i32 s4, 0x1100
	v_mov_b32_e32 v1, 0x18000
	v_mad_u32_u24 v1, v138, s4, v1
	s_mov_b64 s[4:5], -1
	s_waitcnt lgkmcnt(0)
	s_cmp_ge_i32 s2, s3
	v_lshlrev_b32_e32 v130, 4, v0
	s_cbranch_scc0 .LBB6_69
	s_load_dwordx8 s[4:11], s[0:1], 0x0
	s_load_dwordx8 s[12:19], s[0:1], 0x20
	s_load_dwordx2 s[22:23], s[0:1], 0x40
	v_and_b32_e32 v159, 63, v0
	v_lshrrev_b32_e32 v160, 6, v0
	v_and_b32_e32 v143, 3, v159
	v_and_b32_e32 v167, 15, v159
	s_nop 0
	v_readfirstlane_b32 s61, v160
	s_waitcnt lgkmcnt(0)
	s_mov_b64 s[26:27], s[6:7]
	s_mov_b64 s[28:29], s[10:11]
	s_mov_b64 s[24:25], s[14:15]
	s_mov_b64 s[64:65], s[16:17]
	s_mov_b64 s[66:67], s[18:19]
	s_mov_b64 s[68:69], s[8:9]
	s_mov_b32 s8, s4
	s_and_b32 s9, s5, 0xffff
	s_mov_b32 s10, 0x40000000
	s_mov_b32 s11, 0x20000
	s_mov_b32 s12, s68
	s_and_b32 s13, s69, 0xffff
	s_mov_b32 s14, 0x40000000
	s_mov_b32 s15, 0x20000
	s_add_u32 s16, s24, 0x712bd00
	s_addc_u32 s17, s25, 0
	s_add_u32 s18, s16, 0xc35000
	s_addc_u32 s19, s17, 0
	s_add_u32 s20, s16, 0x186a000
	s_addc_u32 s21, s17, 0
	s_sub_u32 s52, s2, 88
	s_mul_i32 s52, s52, 75
	s_mov_b32 s71, s52
	s_add_u32 s32, s52, 75
	s_min_u32 s32, s32, 12500
	s_add_u32 s35, s52, s61
	s_mul_i32 s61, s61, 0x1100
	s_add_u32 s61, s61, 0x18000
	v_lshrrev_b32_e32 v160, 2, v159
	v_lshrrev_b32_e32 v161, 4, v159
	v_lshlrev_b32_e32 v134, 4, v143
	v_mov_b32_e32 v135, v134
	v_mul_u32_u24_e32 v162, 0x110, v160
	v_add3_u32 v136, v162, v134, s61
	v_mul_u32_u24_e32 v162, 0x110, v167
	v_lshl_add_u32 v137, v161, 4, v162
	v_add_u32_e32 v137, s61, v137
	v_lshl_add_u32 v140, v161, 3, v162
	v_add_u32_e32 v140, s61, v140
	v_mul_u32_u24_e32 v162, 0x110, v161
	v_lshl_add_u32 v141, v167, 4, v162
	v_add_u32_e32 v141, s61, v141
	v_lshlrev_b32_e32 v138, 4, v159
	v_add_u32_e32 v139, 0x10000, v138
	v_lshlrev_b32_e32 v142, 8, v161
	v_lshl_add_u32 v142, v167, 4, v142
	v_mov_b32_e32 v144, 0x800000
	v_lshlrev_b32_e32 v145, 2, v160
	v_lshl_add_u32 v145, v143, 6, v145
	v_mul_u32_u24_e32 v146, 0x100, v160
	v_add_u32_e32 v146, v146, v135
	s_lshl_b32 s52, s35, 10
	v_add_u32_e32 v160, s52, v145
	global_load_dword v151, v160, s[16:17]
	global_load_dword v152, v160, s[16:17] offset:256
	global_load_dword v153, v160, s[18:19]
	global_load_dword v154, v160, s[18:19] offset:256
	s_lshl_b32 s52, s35, 2
	v_and_b32_e32 v161, 1, v159
	v_mul_u32_u24_e32 v161, 0xc350, v161
	v_add_u32_e32 v161, s52, v161
	global_load_dword v155, v161, s[20:21]
	s_mov_b32 s40, s64
	s_and_b32 s41, s65, 0xffff
	s_mov_b32 s42, 0x18000
	s_mov_b32 s43, 0x20000
	v_lshlrev_b32_e32 v160, 4, v0
	buffer_load_dwordx4 v[2:5], v160, s[40:43], 0 offen
	v_add_u32_e32 v161, 0x3000, v160
	buffer_load_dwordx4 v[6:9], v161, s[40:43], 0 offen
	v_add_u32_e32 v161, 0x6000, v160
	buffer_load_dwordx4 v[10:13], v161, s[40:43], 0 offen
	v_add_u32_e32 v161, 0x9000, v160
	buffer_load_dwordx4 v[14:17], v161, s[40:43], 0 offen
	v_add_u32_e32 v161, 0xc000, v160
	buffer_load_dwordx4 v[18:21], v161, s[40:43], 0 offen
	v_add_u32_e32 v161, 0xf000, v160
	buffer_load_dwordx4 v[22:25], v161, s[40:43], 0 offen
	v_add_u32_e32 v161, 0x12000, v160
	buffer_load_dwordx4 v[26:29], v161, s[40:43], 0 offen
	v_add_u32_e32 v161, 0x15000, v160
	buffer_load_dwordx4 v[30:33], v161, s[40:43], 0 offen
	v_lshlrev_b32_e32 v162, 2, v0
	v_cmp_gt_u32_e32 vcc, 0x80, v0
	s_and_saveexec_b64 s[58:59], vcc
	s_cbranch_execz .Lfb_nobias
	global_load_dword v163, v162, s[66:67]
.Lfb_nobias:
	s_mov_b64 exec, s[58:59]
	s_waitcnt vmcnt(7)
	ds_write_b128 v160, v[2:5]
	s_waitcnt vmcnt(6)
	v_add_u32_e32 v161, 0x3000, v160
	ds_write_b128 v161, v[6:9]
	s_waitcnt vmcnt(5)
	v_add_u32_e32 v161, 0x6000, v160
	ds_write_b128 v161, v[10:13]
	s_waitcnt vmcnt(4)
	v_add_u32_e32 v161, 0x9000, v160
	ds_write_b128 v161, v[14:17]
	s_waitcnt vmcnt(3)
	v_add_u32_e32 v161, 0xc000, v160
	ds_write_b128 v161, v[18:21]
	s_waitcnt vmcnt(2)
	v_add_u32_e32 v161, 0xf000, v160
	ds_write_b128 v161, v[22:25]
	s_waitcnt vmcnt(1)
	v_add_u32_e32 v161, 0x12000, v160
	ds_write_b128 v161, v[26:29]
	s_waitcnt vmcnt(0)
	v_add_u32_e32 v161, 0x15000, v160
	ds_write_b128 v161, v[30:33]
	s_waitcnt vmcnt(0)
	v_cmp_gt_u32_e32 vcc, 0x80, v0
	s_and_saveexec_b64 s[58:59], vcc
	v_add_u32_e32 v162, 0x24c00, v162
	ds_write_b32 v162, v163
	s_mov_b64 exec, s[58:59]
	v_cmp_eq_u32_e32 vcc, 0, v0
	s_and_saveexec_b64 s[58:59], vcc
	v_mov_b32_e32 v160, 0x24e00
	s_add_u32 s53, s71, 12
	v_mov_b32_e32 v161, s53
	ds_write_b32 v160, v161
	s_mov_b64 exec, s[58:59]
	s_waitcnt lgkmcnt(0)
	s_barrier
	s_waitcnt vmcnt(0)
	s_mov_b32 s34, s35
	v_readlane_b32 s52, v155, 0
	v_readlane_b32 s53, v155, 1
	s_cmp_lt_u32 s34, s32
	s_cselect_b32 s47, s52, 0
	s_cselect_b32 s48, s53, 0
	s_max_u32 s38, s47, 2
	s_max_u32 s39, s48, 2
	v_cmp_gt_i32_e32 vcc, s47, v143
	s_nop 1
	v_cndmask_b32_e32 v147, v144, v151, vcc
	v_mov_b32_e32 v148, v152
	v_mov_b32_e32 v149, v153
	v_mov_b32_e32 v150, v154
	s_mov_b32 s44, 0
	s_mov_b32 s46, 0
	s_mov_b32 s45, s38
	s_mov_b64 s[40:41], s[8:9]
	s_mov_b64 s[42:43], s[10:11]
	s_movk_i32 s49, 0x100
	s_mov_b32 s70, 0
	v_mov_b32_e32 v160, 1
	v_mov_b32_e32 v161, 0x24e00
	s_mov_b64 s[58:59], exec
	s_mov_b64 exec, 1
	ds_add_rtn_u32 v160, v161, v160
	s_waitcnt lgkmcnt(0)
	v_readfirstlane_b32 s35, v160
	s_mov_b64 exec, s[58:59]
	s_lshl_b32 s52, s35, 10
	v_add_u32_e32 v160, s52, v145
	global_load_dword v151, v160, s[16:17]
	global_load_dword v152, v160, s[16:17] offset:256
	global_load_dword v153, v160, s[18:19]
	global_load_dword v154, v160, s[18:19] offset:256
	s_lshl_b32 s52, s35, 2
	v_and_b32_e32 v161, 1, v159
	v_mul_u32_u24_e32 v161, 0xc350, v161
	v_add_u32_e32 v161, s52, v161
	global_load_dword v155, v161, s[20:21]
	s_mov_b32 s64, 2
	s_mov_b32 s66, 0

amdhsa.kernels:
  - .agpr_count:     0
    .args:
      - .actual_access:  read_only
        .address_space:  global
        .offset:         0
        .size:           8
        .value_kind:     global_buffer
      - .actual_access:  read_only
        .address_space:  global
        .offset:         8
        .size:           8
        .value_kind:     global_buffer
      - .actual_access:  write_only
        .address_space:  global
        .offset:         16
        .size:           8
        .value_kind:     global_buffer
      - .address_space:  global
        .offset:         24
        .size:           8
        .value_kind:     global_buffer
    .group_segment_fixed_size: 16400
    .kernarg_segment_align: 8
    .kernarg_segment_size: 32
    .language:       OpenCL C
    .language_version:
      - 2
      - 0
    .max_flat_workgroup_size: 256
    .name:           _Z6k_bcsrPK15HIP_vector_typeIiLj2EEPKiPiS5_
    .private_segment_fixed_size: 0
    .sgpr_count:     28
    .sgpr_spill_count: 0
    .symbol:         _Z6k_bcsrPK15HIP_vector_typeIiLj2EEPKiPiS5_.kd
    .uniform_work_group_size: 1
    .uses_dynamic_stack: false
    .vgpr_count:     28
    .vgpr_spill_count: 0
    .wavefront_size: 64
  - .agpr_count:     0
    .args:
      - .actual_access:  read_only
        .address_space:  global
        .offset:         0
        .size:           8
        .value_kind:     global_buffer
      - .actual_access:  read_only
        .address_space:  global
        .offset:         8
        .size:           8
        .value_kind:     global_buffer
      - .actual_access:  read_only
        .address_space:  global
        .offset:         16
        .size:           8
        .value_kind:     global_buffer
      - .actual_access:  write_only
        .address_space:  global
        .offset:         24
        .size:           8
        .value_kind:     global_buffer
      - .actual_access:  write_only
        .address_space:  global
        .offset:         32
        .size:           8
        .value_kind:     global_buffer
      - .actual_access:  read_only
        .address_space:  global
        .offset:         40
        .size:           8
        .value_kind:     global_buffer
      - .actual_access:  read_only
        .address_space:  global
        .offset:         48
        .size:           8
        .value_kind:     global_buffer
      - .actual_access:  read_only
        .address_space:  global
        .offset:         56
        .size:           8
        .value_kind:     global_buffer
      - .actual_access:  read_only
        .address_space:  global
        .offset:         64
        .size:           8
        .value_kind:     global_buffer
      - .actual_access:  read_only
        .address_space:  global
        .offset:         72
        .size:           8
        .value_kind:     global_buffer
      - .actual_access:  read_only
        .address_space:  global
        .offset:         80
        .size:           8
        .value_kind:     global_buffer
      - .actual_access:  read_only
        .address_space:  global
        .offset:         88
        .size:           8
        .value_kind:     global_buffer
      - .actual_access:  read_only
        .address_space:  global
        .offset:         96
        .size:           8
        .value_kind:     global_buffer
      - .address_space:  global
        .offset:         104
        .size:           8
        .value_kind:     global_buffer
      - .address_space:  global
        .offset:         112
        .size:           8
        .value_kind:     global_buffer
    .group_segment_fixed_size: 4384
    .kernarg_segment_align: 8
    .kernarg_segment_size: 120
    .language:       OpenCL C
    .language_version:
      - 2
      - 0
    .max_flat_workgroup_size: 1024
    .name:           _Z8k_bcountPKiS0_S0_PiPjPKfS4_S0_S0_S0_S4_S4_S4_PDF16_S5_
    .private_segment_fixed_size: 0
    .sgpr_count:     26
    .sgpr_spill_count: 0
    .symbol:         _Z8k_bcountPKiS0_S0_PiPjPKfS4_S0_S0_S0_S4_S4_S4_PDF16_S5_.kd
    .uniform_work_group_size: 1
    .uses_dynamic_stack: false
    .vgpr_count:     41
    .vgpr_spill_count: 0
    .wavefront_size: 64
  - .agpr_count:     0
    .args:
      - .actual_access:  read_only
        .address_space:  global
        .offset:         0
        .size:           8
        .value_kind:     global_buffer
      - .actual_access:  read_only
        .address_space:  global
        .offset:         8
        .size:           8
        .value_kind:     global_buffer
      - .actual_access:  read_only
        .address_space:  global
        .offset:         16
        .size:           8
        .value_kind:     global_buffer
      - .actual_access:  read_only
        .address_space:  global
        .offset:         24
        .size:           8
        .value_kind:     global_buffer
      - .actual_access:  write_only
        .address_space:  global
        .offset:         32
        .size:           8
        .value_kind:     global_buffer
      - .actual_access:  write_only
        .address_space:  global
        .offset:         40
        .size:           8
        .value_kind:     global_buffer
      - .actual_access:  read_only
        .address_space:  global
        .offset:         48
        .size:           8
        .value_kind:     global_buffer
      - .actual_access:  read_only
        .address_space:  global
        .offset:         56
        .size:           8
        .value_kind:     global_buffer
      - .actual_access:  read_only
        .address_space:  global
        .offset:         64
        .size:           8
        .value_kind:     global_buffer
      - .actual_access:  read_only
        .address_space:  global
        .offset:         72
        .size:           8
        .value_kind:     global_buffer
      - .actual_access:  read_only
        .address_space:  global
        .offset:         80
        .size:           8
        .value_kind:     global_buffer
      - .actual_access:  read_only
        .address_space:  global
        .offset:         88
        .size:           8
        .value_kind:     global_buffer
      - .actual_access:  read_only
        .address_space:  global
        .offset:         96
        .size:           8
        .value_kind:     global_buffer
      - .actual_access:  read_only
        .address_space:  global
        .offset:         104
        .size:           8
        .value_kind:     global_buffer
      - .address_space:  global
        .offset:         112
        .size:           8
        .value_kind:     global_buffer
      - .address_space:  global
        .offset:         120
        .size:           8
        .value_kind:     global_buffer
      - .offset:         128
        .size:           488
        .value_kind:     by_value
    .group_segment_fixed_size: 17024
    .kernarg_segment_align: 8
    .kernarg_segment_size: 616
    .language:       OpenCL C
    .language_version:
      - 2
      - 0
    .max_flat_workgroup_size: 1024
    .name:           _Z6k_prepPKiS0_S0_S0_PiP15HIP_vector_typeIiLj2EEPKfS6_S0_S0_S0_S6_S6_S6_PDF16_S7_6WSpecs
    .private_segment_fixed_size: 0
    .sgpr_count:     44
    .sgpr_spill_count: 0
    .symbol:         _Z6k_prepPKiS0_S0_S0_PiP15HIP_vector_typeIiLj2EEPKfS6_S0_S0_S0_S6_S6_S6_PDF16_S7_6WSpecs.kd
    .uniform_work_group_size: 1
    .uses_dynamic_stack: false
    .vgpr_count:     82
    .vgpr_spill_count: 0
    .wavefront_size: 64
  - .agpr_count:     0
    .args:
      - .offset:         0
        .size:           104
        .value_kind:     by_value
      - .offset:         104
        .size:           4
        .value_kind:     hidden_block_count_x
      - .offset:         108
        .size:           4
        .value_kind:     hidden_block_count_y
      - .offset:         112
        .size:           4
        .value_kind:     hidden_block_count_z
      - .offset:         116
        .size:           2
        .value_kind:     hidden_group_size_x
      - .offset:         118
        .size:           2
        .value_kind:     hidden_group_size_y
      - .offset:         120
        .size:           2
        .value_kind:     hidden_group_size_z
      - .offset:         122
        .size:           2
        .value_kind:     hidden_remainder_x
      - .offset:         124
        .size:           2
        .value_kind:     hidden_remainder_y
      - .offset:         126
        .size:           2
        .value_kind:     hidden_remainder_z
      - .offset:         144
        .size:           8
        .value_kind:     hidden_global_offset_x
      - .offset:         152
        .size:           8
        .value_kind:     hidden_global_offset_y
      - .offset:         160
        .size:           8
        .value_kind:     hidden_global_offset_z
      - .offset:         168
        .size:           2
        .value_kind:     hidden_grid_dims
    .group_segment_fixed_size: 155140
    .kernarg_segment_align: 8
    .kernarg_segment_size: 360
    .language:       OpenCL C
    .language_version:
      - 2
      - 0
    .max_flat_workgroup_size: 768
    .name:           _Z12k_layer_pool9LayerArgs
    .private_segment_fixed_size: 0
    .sgpr_count:     50
    .sgpr_spill_count: 0
    .symbol:         _Z12k_layer_pool9LayerArgs.kd
    .uniform_work_group_size: 1
    .uses_dynamic_stack: false
    .vgpr_count:     168
    .vgpr_spill_count: 0
    .wavefront_size: 64
  - .agpr_count:     0
    .args:
      - .actual_access:  read_only
        .address_space:  global
        .offset:         0
        .size:           8
        .value_kind:     global_buffer
      - .actual_access:  read_only
        .address_space:  global
        .offset:         8
        .size:           8
        .value_kind:     global_buffer
      - .actual_access:  read_only
        .address_space:  global
        .offset:         16
        .size:           8
        .value_kind:     global_buffer
      - .actual_access:  read_only
        .address_space:  global
        .offset:         24
        .size:           8
        .value_kind:     global_buffer
      - .actual_access:  read_only
        .address_space:  global
        .offset:         32
        .size:           8
        .value_kind:     global_buffer
      - .actual_access:  read_only
        .address_space:  global
        .offset:         40
        .size:           8
        .value_kind:     global_buffer
      - .actual_access:  read_only
        .address_space:  global
        .offset:         48
        .size:           8
        .value_kind:     global_buffer
      - .actual_access:  write_only
        .address_space:  global
        .offset:         56
        .size:           8
        .value_kind:     global_buffer
    .group_segment_fixed_size: 2560
    .kernarg_segment_align: 8
    .kernarg_segment_size: 64
    .language:       OpenCL C
    .language_version:
      - 2
      - 0
    .max_flat_workgroup_size: 512
    .name:           _Z5k_mlpPKjPKfS2_S2_S2_S2_S2_Pf
    .private_segment_fixed_size: 0
    .sgpr_count:     18
    .sgpr_spill_count: 0
    .symbol:         _Z5k_mlpPKjPKfS2_S2_S2_S2_S2_Pf.kd
    .uniform_work_group_size: 1
    .uses_dynamic_stack: false
    .vgpr_count:     120
    .vgpr_spill_count: 0
    .wavefront_size: 64
  - .agpr_count:     0
    .args:
      - .offset:         0
        .size:           104
        .value_kind:     by_value
      - .offset:         104
        .size:           104
        .value_kind:     by_value
      - .offset:         208
        .size:           4
        .value_kind:     by_value
      - .offset:         216
        .size:           4
        .value_kind:     hidden_block_count_x
      - .offset:         220
        .size:           4
        .value_kind:     hidden_block_count_y
      - .offset:         224
        .size:           4
        .value_kind:     hidden_block_count_z
      - .offset:         228
        .size:           2
        .value_kind:     hidden_group_size_x
      - .offset:         230
        .size:           2
        .value_kind:     hidden_group_size_y
      - .offset:         232
        .size:           2
        .value_kind:     hidden_group_size_z
      - .offset:         234
        .size:           2
        .value_kind:     hidden_remainder_x
      - .offset:         236
        .size:           2
        .value_kind:     hidden_remainder_y
      - .offset:         238
        .size:           2
        .value_kind:     hidden_remainder_z
      - .offset:         256
        .size:           8
        .value_kind:     hidden_global_offset_x
      - .offset:         264
        .size:           8
        .value_kind:     hidden_global_offset_y
      - .offset:         272
        .size:           8
        .value_kind:     hidden_global_offset_z
      - .offset:         280
        .size:           2
        .value_kind:     hidden_grid_dims
    .group_segment_fixed_size: 151044
    .kernarg_segment_align: 8
    .kernarg_segment_size: 472
    .language:       OpenCL C
    .language_version:
      - 2
      - 0
    .max_flat_workgroup_size: 768
    .name:           _Z10k_layer_fhILi96ELb1EEv9LayerArgsS0_i
    .private_segment_fixed_size: 0
    .sgpr_count:     52
    .sgpr_spill_count: 0
    .symbol:         _Z10k_layer_fhILi96ELb1EEv9LayerArgsS0_i.kd
    .uniform_work_group_size: 1
    .uses_dynamic_stack: false
    .vgpr_count:     168
    .vgpr_spill_count: 0
    .wavefront_size: 64
  - .agpr_count:     0
    .args:
      - .offset:         0
        .size:           104
        .value_kind:     by_value
      - .offset:         104
        .size:           104
        .value_kind:     by_value
      - .offset:         208
        .size:           4
        .value_kind:     by_value
      - .offset:         216
        .size:           4
        .value_kind:     hidden_block_count_x
      - .offset:         220
        .size:           4
        .value_kind:     hidden_block_count_y
      - .offset:         224
        .size:           4
        .value_kind:     hidden_block_count_z
      - .offset:         228
        .size:           2
        .value_kind:     hidden_group_size_x
      - .offset:         230
        .size:           2
        .value_kind:     hidden_group_size_y
      - .offset:         232
        .size:           2
        .value_kind:     hidden_group_size_z
      - .offset:         234
        .size:           2
        .value_kind:     hidden_remainder_x
      - .offset:         236
        .size:           2
        .value_kind:     hidden_remainder_y
      - .offset:         238
        .size:           2
        .value_kind:     hidden_remainder_z
      - .offset:         256
        .size:           8
        .value_kind:     hidden_global_offset_x
      - .offset:         264
        .size:           8
        .value_kind:     hidden_global_offset_y
      - .offset:         272
        .size:           8
        .value_kind:     hidden_global_offset_z
      - .offset:         280
        .size:           2
        .value_kind:     hidden_grid_dims
    .group_segment_fixed_size: 151044
    .kernarg_segment_align: 8
    .kernarg_segment_size: 472
    .language:       OpenCL C
    .language_version:
      - 2
      - 0
    .max_flat_workgroup_size: 768
    .name:           _Z10k_layer_fhILi128ELb1EEv9LayerArgsS0_i
    .private_segment_fixed_size: 0
    .sgpr_count:     45
    .sgpr_spill_count: 0
    .symbol:         _Z10k_layer_fhILi128ELb1EEv9LayerArgsS0_i.kd
    .uniform_work_group_size: 1
    .uses_dynamic_stack: false
    .vgpr_count:     168
    .vgpr_spill_count: 0
    .wavefront_size: 64
